# speedup vs baseline: 1.0056x; 1.0056x over previous
.LBB1_3:
	v_mov_b32_e32 v156, v0
	s_nop 0
	v_ashrrev_i32_e32 v157, 31, v156
	v_and_b32_e32 v167, 63, v156
	v_lshl_add_u64 v[6:7], v[156:157], 3, s[10:11]
	v_lshlrev_b32_e32 v169, 3, v167
	global_load_dwordx2 v[4:5], v[6:7], off
	global_load_dwordx2 v[2:3], v169, s[10:11] offset:2048
	v_readfirstlane_b32 s4, v156
	s_ashr_i32 s27, s4, 7
	s_lshl_b32 s0, s27, 1
	s_ashr_i32 s1, s0, 31
	s_lshl_b64 s[2:3], s[0:1], 13
	s_add_u32 s2, s8, s2
	s_addc_u32 s3, s9, s3
	s_add_u32 s28, s2, 0x18000
	s_addc_u32 s29, s3, 0
	v_lshlrev_b32_e32 v154, 4, v167
	v_lshl_add_u64 v[6:7], s[28:29], 0, v[154:155]
	v_or_b32_e32 v8, 0x800, v169
	v_add_co_u32_e32 v6, vcc, s23, v6
	v_lshlrev_b32_e32 v168, 1, v8
	s_nop 0
	v_addc_co_u32_e32 v7, vcc, 0, v7, vcc
	v_lshl_add_u64 v[8:9], s[6:7], 0, v[154:155]
	global_load_dwordx4 v[150:153], v154, s[28:29]
	global_load_dwordx4 v[146:149], v154, s[28:29] offset:1024
	global_load_dwordx4 v[142:145], v154, s[28:29] offset:2048
	global_load_dwordx4 v[138:141], v154, s[28:29] offset:3072
	global_load_dwordx4 v[126:129], v[6:7], off offset:1024
	global_load_dwordx4 v[122:125], v[6:7], off offset:2048
	global_load_dwordx4 v[118:121], v154, s[6:7]
	global_load_dwordx4 v[114:117], v154, s[6:7] offset:1024
	global_load_dwordx4 v[110:113], v154, s[6:7] offset:2048
	global_load_dwordx4 v[106:109], v154, s[6:7] offset:3072
	global_load_dwordx4 v[134:137], v168, s[28:29]
	global_load_dwordx4 v[102:105], v168, s[6:7]
	v_add_co_u32_e32 v8, vcc, s23, v8
	s_nop 1
	v_addc_co_u32_e32 v9, vcc, 0, v9, vcc
	global_load_dwordx4 v[130:133], v[6:7], off offset:3072
	global_load_dwordx4 v[98:101], v[8:9], off offset:1024
	global_load_dwordx4 v[94:97], v[8:9], off offset:2048
	global_load_dwordx4 v[90:93], v[8:9], off offset:3072
	v_lshl_add_u64 v[6:7], s[2:3], 0, v[154:155]
	v_lshl_add_u64 v[8:9], v[6:7], 0, s[16:17]
	v_add_co_u32_e32 v6, vcc, 0x28000, v6
	s_nop 1
	v_addc_co_u32_e32 v7, vcc, 0, v7, vcc
	global_load_dwordx4 v[86:89], v[6:7], off
	global_load_dwordx4 v[82:85], v[8:9], off offset:1024
	v_lshrrev_b32_e32 v182, 5, v167
	s_ashr_i32 s2, s4, 6
	s_lshl_b32 s3, s2, 3
	s_and_b32 s5, s3, 8
	s_bfe_u32 s26, s2, 0x10001
	s_or_b32 s5, s26, s5
	s_lshl_b32 s26, s2, 9
	s_and_b32 s26, s26, 0x400
	s_lshl_b32 s5, s5, 4
	s_or_b32 s28, s5, s26
	v_bfe_u32 v76, v156, 4, 1
	v_bitop3_b32 v77, v182, v156, 1 bitop3:0x78
	v_lshlrev_b32_e32 v154, 2, v182
	v_xor_b32_e32 v77, v77, v76
	v_bitop3_b32 v78, v154, v156, 4 bitop3:0x78
	v_and_b32_e32 v79, 10, v156
	v_or3_b32 v77, v79, v78, v77
	s_lshl_b32 s5, s2, 4
	v_lshlrev_b32_e32 v77, 4, v77
	s_lshl_b32 s3, s2, 13
	s_and_b32 s29, s5, 16
	v_lshlrev_b32_e32 v170, 8, v182
	v_lshl_or_b32 v171, v76, 10, v77
	s_or_b32 s26, s29, s3
	v_bitop3_b32 v179, v171, s26, v170 bitop3:0x36
	s_or_b32 s5, s26, 0x280
	v_bitop3_b32 v178, v171, s5, v170 bitop3:0x36
	s_or_b32 s30, s3, 0x800
	s_or_b32 s33, s3, 0x1000
	s_or_b32 s29, s29, 64
	s_or_b32 s34, s29, s33
	v_bitop3_b32 v180, v171, s34, v170 bitop3:0x36
	s_or_b32 s29, s3, s29
	s_or_b32 s29, s29, 0x1280
	s_and_b32 s5, s2, 1
	s_lshl_b32 s31, s5, 4
	s_or_b32 s2, s31, s3
	v_bitop3_b32 v173, v171, s2, v170 bitop3:0x36
	v_bitop3_b32 v76, v156, 31, v156 bitop3:0xc
	v_lshrrev_b32_e32 v77, 4, v76
	v_bitop3_b32 v78, v76, v182, 1 bitop3:0x6c
	v_xor_b32_e32 v78, v78, v77
	v_bitop3_b32 v76, v76, v154, 4 bitop3:0x6c
	v_bitop3_b32 v79, v156, 10, 31 bitop3:8
	v_or3_b32 v76, v79, v76, v78
	v_lshlrev_b32_e32 v77, 10, v77
	v_lshlrev_b32_e32 v76, 4, v76
	v_or3_b32 v154, v77, v76, v170
	v_bitop3_b32 v172, s2, v154, v159 bitop3:0x36
	v_bitop3_b32 v176, v171, s29, v170 bitop3:0x36
	s_or_b32 s29, s31, s30
	s_or_b32 s29, s29, 0xa0
	v_bitop3_b32 v175, v171, s29, v170 bitop3:0x36
	s_or_b32 s29, s2, 0xaa0
	s_xor_b32 s29, s29, 0x80
	v_xor_b32_e32 v174, s29, v154
	s_or_b32 s29, s26, 0x18e0
	v_bitop3_b32 v181, v171, s29, v170 bitop3:0x36
	s_or_b32 s29, s26, 0x1a60
	v_bitop3_b32 v177, v171, s29, v170 bitop3:0x36
	s_or_b32 s29, s31, 64
	s_or_b32 s3, s3, s29
	s_mov_b32 s41, s3
	s_or_b32 s29, s29, s33
	s_mov_b32 s40, s29
	s_or_b32 s3, s2, 0x18e0
	s_mov_b32 s42, s3
	s_or_b32 s2, s2, 0x1ae0
	s_xor_b32 s2, s2, 0x80
	s_mov_b32 s43, s2
	v_cmp_gt_i32_e32 vcc, 16, v156
	v_lshl_add_u32 v166, v156, 2, v165
	s_and_saveexec_b64 s[2:3], vcc
	ds_write_b32 v166, v155
	s_or_b64 exec, exec, s[2:3]
	v_lshl_add_u32 v6, v156, 3, v1
	v_cmp_gt_i32_e32 vcc, 64, v156
	s_waitcnt vmcnt(19)
	ds_write_b64 v6, v[4:5]
	s_and_saveexec_b64 s[2:3], vcc
	s_cbranch_execz .LBB1_7
	s_waitcnt vmcnt(18)
	ds_write_b64 v6, v[2:3] offset:2048
.LBB1_7:
	s_or_b64 exec, exec, s[2:3]
	v_mov_b32_e32 v10, v167
	s_waitcnt lgkmcnt(0)
	s_barrier
	s_waitcnt vmcnt(18)
	s_lshr_b32 s38, s4, 1
	v_and_b32_e32 v26, 31, v167
	v_and_b32_e32 v27, 3, v167
	v_bfe_u32 v28, v167, 3, 1
	v_bfe_u32 v29, v167, 2, 1
	v_lshl_or_b32 v27, v28, 2, v27
	v_lshl_or_b32 v27, v29, 3, v27
	v_lshlrev_b32_e32 v32, 9, v182
	v_lshl_add_u32 v30, v27, 3, v32
	v_add_u32_e32 v30, 0x10000, v30
	v_lshl_add_u32 v31, v26, 3, v32
	v_add_u32_e32 v31, 0x10400, v31
	v_xor_b32_e32 v28, 31, v26
	v_lshl_add_u32 v28, v28, 3, v32
	v_add_u32_e32 v28, 0x10400, v28
	v_bfe_u32 v29, v167, 4, 1
	v_mul_u32_u24_e32 v29, 0x78, v29
	v_xor_b32_e32 v254, s38, v29
	v_or_b32_e32 v254, 0x10800, v254
	v_and_b32_e32 v33, 16, v167
	v_cmp_eq_u32_e32 vcc, 0, v33
	ds_read2_b64 v[66:69], v30 offset0:0 offset1:32
	ds_read2_b64 v[70:73], v30 offset0:16 offset1:48
	ds_read2_b64 v[230:233], v31 offset0:0 offset1:32
	ds_read2_b64 v[234:237], v28 offset0:0 offset1:32
	ds_read2_b64 v[238:241], v254 offset0:0 offset1:16
	ds_read2_b64 v[242:245], v254 offset0:32 offset1:48
	s_waitcnt lgkmcnt(0)
	v_cndmask_b32_e32 v74, v67, v66, vcc
	v_cndmask_b32_e32 v75, v69, v68, vcc
	v_cndmask_b32_e64 v76, v66, -v67, vcc
	v_cndmask_b32_e64 v77, v68, -v69, vcc
	v_cndmask_b32_e32 v78, v71, v70, vcc
	v_cndmask_b32_e32 v79, v73, v72, vcc
	v_cndmask_b32_e64 v80, v70, -v71, vcc
	v_cndmask_b32_e64 v81, v72, -v73, vcc
	v_cvt_pk_f16_f32 v222, v74, v75
	v_cvt_pk_f16_f32 v223, v74, v75
	v_cvt_pk_f16_f32 v224, v76, v77
	v_cvt_pk_f16_f32 v225, v76, v77
	v_cvt_pk_f16_f32 v226, v78, v79
	v_cvt_pk_f16_f32 v227, v78, v79
	v_cvt_pk_f16_f32 v228, v80, v81
	v_cvt_pk_f16_f32 v229, v80, v81
	v_mul_f32_e32 v66, v231, v239
	v_mul_f32_e32 v68, v231, v238
	v_mul_f32_e32 v67, v231, v241
	v_mul_f32_e32 v69, v231, v240
	v_fma_f32 v66, v230, v238, -v66
	v_fma_f32 v68, v230, v239, v68
	v_fma_f32 v67, v230, v240, -v67
	v_fma_f32 v69, v230, v241, v69
	v_cvt_pk_f16_f32 v246, v66, v67
	v_cvt_pk_f16_f32 v248, v68, v69
	v_mul_f32_e32 v70, v233, v243
	v_mul_f32_e32 v72, v233, v242
	v_mul_f32_e32 v71, v233, v245
	v_mul_f32_e32 v73, v233, v244
	v_fma_f32 v70, v232, v242, -v70
	v_fma_f32 v72, v232, v243, v72
	v_fma_f32 v71, v232, v244, -v71
	v_fma_f32 v73, v232, v245, v73
	v_cvt_pk_f16_f32 v247, v70, v71
	v_cvt_pk_f16_f32 v249, v72, v73
	v_mul_f32_e32 v66, v235, v239
	v_mul_f32_e32 v68, v235, v238
	v_mul_f32_e32 v67, v235, v241
	v_mul_f32_e32 v69, v235, v240
	v_fma_f32 v66, v234, v238, -v66
	v_fma_f32 v68, v234, v239, v68
	v_fma_f32 v67, v234, v240, -v67
	v_fma_f32 v69, v234, v241, v69
	v_cvt_pk_f16_f32 v250, v66, v67
	v_cvt_pk_f16_f32 v252, v68, v69
	v_mul_f32_e32 v70, v237, v243
	v_mul_f32_e32 v72, v237, v242
	v_mul_f32_e32 v71, v237, v245
	v_mul_f32_e32 v73, v237, v244
	v_fma_f32 v70, v236, v242, -v70
	v_fma_f32 v72, v236, v243, v72
	v_fma_f32 v71, v236, v244, -v71
	v_fma_f32 v73, v236, v245, v73
	v_cvt_pk_f16_f32 v251, v70, v71
	v_cvt_pk_f16_f32 v253, v72, v73
	v_xor_b32_e32 v255, 8, v254
	ds_read2_b64 v[238:241], v255 offset0:0 offset1:16
	ds_read2_b64 v[242:245], v255 offset0:32 offset1:48
	v_mfma_f32_32x32x16_f16 v[2:17], v[222:225], v[246:249], 0
	v_mfma_f32_32x32x16_f16 v[18:33], v[226:229], v[250:253], 0
	s_waitcnt lgkmcnt(0)
	v_mul_f32_e32 v66, v231, v239
	v_mul_f32_e32 v68, v231, v238
	v_mul_f32_e32 v67, v231, v241
	v_mul_f32_e32 v69, v231, v240
	v_fma_f32 v66, v230, v238, -v66
	v_fma_f32 v68, v230, v239, v68
	v_fma_f32 v67, v230, v240, -v67
	v_fma_f32 v69, v230, v241, v69
	v_cvt_pk_f16_f32 v246, v66, v67
	v_cvt_pk_f16_f32 v248, v68, v69
	v_mul_f32_e32 v70, v233, v243
	v_mul_f32_e32 v72, v233, v242
	v_mul_f32_e32 v71, v233, v245
	v_mul_f32_e32 v73, v233, v244
	v_fma_f32 v70, v232, v242, -v70
	v_fma_f32 v72, v232, v243, v72
	v_fma_f32 v71, v232, v244, -v71
	v_fma_f32 v73, v232, v245, v73
	v_cvt_pk_f16_f32 v247, v70, v71
	v_cvt_pk_f16_f32 v249, v72, v73
	v_cvt_pk_f16_f32 v2, v2, v3
	v_cvt_pk_f16_f32 v3, v4, v5
	v_cvt_pk_f16_f32 v4, v6, v7
	v_cvt_pk_f16_f32 v5, v8, v9
	v_cvt_pk_f16_f32 v6, v10, v11
	v_cvt_pk_f16_f32 v7, v12, v13
	v_cvt_pk_f16_f32 v8, v14, v15
	v_cvt_pk_f16_f32 v9, v16, v17
	v_cvt_pk_f16_f32 v18, v18, v19
	v_cvt_pk_f16_f32 v19, v20, v21
	v_cvt_pk_f16_f32 v20, v22, v23
	v_cvt_pk_f16_f32 v21, v24, v25
	v_cvt_pk_f16_f32 v22, v26, v27
	v_cvt_pk_f16_f32 v23, v28, v29
	v_cvt_pk_f16_f32 v24, v30, v31
	v_cvt_pk_f16_f32 v25, v32, v33
	s_setprio 1
	s_waitcnt vmcnt(14)
	v_mul_f32_e32 v66, v235, v239
	v_mul_f32_e32 v68, v235, v238
	v_mfma_f32_32x32x16_f16 v[34:49], v[2:5], v[150:153], 0
	v_mul_f32_e32 v67, v235, v241
	v_mul_f32_e32 v69, v235, v240
	v_mfma_f32_32x32x16_f16 v[34:49], v[18:21], v[146:149], v[34:49]
	v_fma_f32 v66, v234, v238, -v66
	v_fma_f32 v68, v234, v239, v68
	v_mfma_f32_32x32x16_f16 v[34:49], v[6:9], v[142:145], v[34:49]
	v_fma_f32 v67, v234, v240, -v67
	v_fma_f32 v69, v234, v241, v69
	v_mfma_f32_32x32x16_f16 v[34:49], v[22:25], v[138:141], v[34:49]
	v_cvt_pk_f16_f32 v250, v66, v67
	v_cvt_pk_f16_f32 v252, v68, v69
	s_waitcnt vmcnt(5)
	v_mul_f32_e32 v70, v237, v243
	v_mul_f32_e32 v72, v237, v242
	v_mfma_f32_32x32x16_f16 v[50:65], v[2:5], v[134:137], 0
	v_mul_f32_e32 v71, v237, v245
	v_mul_f32_e32 v73, v237, v244
	v_mfma_f32_32x32x16_f16 v[50:65], v[18:21], v[126:129], v[50:65]
	v_fma_f32 v70, v236, v242, -v70
	v_fma_f32 v72, v236, v243, v72
	v_mfma_f32_32x32x16_f16 v[50:65], v[6:9], v[122:125], v[50:65]
	v_fma_f32 v71, v236, v244, -v71
	v_fma_f32 v73, v236, v245, v73
	v_mfma_f32_32x32x16_f16 v[50:65], v[22:25], v[130:133], v[50:65]
	v_cvt_pk_f16_f32 v251, v70, v71
	v_cvt_pk_f16_f32 v253, v72, v73
	v_xor_b32_e32 v255, 16, v254
	ds_read2_b64 v[238:241], v255 offset0:0 offset1:16
	ds_read2_b64 v[242:245], v255 offset0:32 offset1:48
	v_mfma_f32_32x32x16_f16 v[2:17], v[222:225], v[246:249], 0
	v_mfma_f32_32x32x16_f16 v[18:33], v[226:229], v[250:253], 0
	v_cvt_pk_f16_f32 v34, v34, v35
	v_cvt_pk_f16_f32 v35, v36, v37
	v_cvt_pk_f16_f32 v36, v38, v39
	v_cvt_pk_f16_f32 v37, v40, v41
	v_cvt_pk_f16_f32 v38, v42, v43
	v_cvt_pk_f16_f32 v39, v44, v45
	v_cvt_pk_f16_f32 v40, v46, v47
	v_cvt_pk_f16_f32 v41, v48, v49
	v_cvt_pk_f16_f32 v50, v50, v51
	v_cvt_pk_f16_f32 v51, v52, v53
	v_cvt_pk_f16_f32 v52, v54, v55
	v_cvt_pk_f16_f32 v53, v56, v57
	v_cvt_pk_f16_f32 v54, v58, v59
	v_cvt_pk_f16_f32 v55, v60, v61
	v_cvt_pk_f16_f32 v56, v62, v63
	v_cvt_pk_f16_f32 v57, v64, v65
	s_waitcnt vmcnt(2)
	v_cvt_pk_f16_f32 v2, v2, v3
	v_cvt_pk_f16_f32 v3, v4, v5
	v_cvt_pk_f16_f32 v4, v6, v7
	v_cvt_pk_f16_f32 v5, v8, v9
	v_mfma_f32_32x32x16_f16 v[190:205], v[34:37], v[118:121], 0
	v_cvt_pk_f16_f32 v6, v10, v11
	v_cvt_pk_f16_f32 v7, v12, v13
	v_cvt_pk_f16_f32 v8, v14, v15
	v_cvt_pk_f16_f32 v9, v16, v17
	v_mfma_f32_32x32x16_f16 v[206:221], v[34:37], v[102:105], 0
	v_cvt_pk_f16_f32 v18, v18, v19
	v_cvt_pk_f16_f32 v19, v20, v21
	v_cvt_pk_f16_f32 v20, v22, v23
	v_cvt_pk_f16_f32 v21, v24, v25
	v_mfma_f32_32x32x16_f16 v[190:205], v[38:41], v[114:117], v[190:205]
	v_cvt_pk_f16_f32 v22, v26, v27
	v_cvt_pk_f16_f32 v23, v28, v29
	v_cvt_pk_f16_f32 v24, v30, v31
	v_cvt_pk_f16_f32 v25, v32, v33
	v_mfma_f32_32x32x16_f16 v[206:221], v[38:41], v[98:101], v[206:221]
	s_waitcnt lgkmcnt(0)
	v_mul_f32_e32 v66, v231, v239
	v_mul_f32_e32 v68, v231, v238
	v_mul_f32_e32 v67, v231, v241
	v_mfma_f32_32x32x16_f16 v[190:205], v[50:53], v[110:113], v[190:205]
	v_mul_f32_e32 v69, v231, v240
	v_fma_f32 v66, v230, v238, -v66
	v_fma_f32 v68, v230, v239, v68
	v_fma_f32 v67, v230, v240, -v67
	v_mfma_f32_32x32x16_f16 v[206:221], v[50:53], v[94:97], v[206:221]
	v_fma_f32 v69, v230, v241, v69
	v_cvt_pk_f16_f32 v246, v66, v67
	v_cvt_pk_f16_f32 v248, v68, v69
	v_mul_f32_e32 v70, v233, v243
	v_mfma_f32_32x32x16_f16 v[190:205], v[54:57], v[106:109], v[190:205]
	v_mul_f32_e32 v72, v233, v242
	v_mul_f32_e32 v71, v233, v245
	v_mul_f32_e32 v73, v233, v244
	v_fma_f32 v70, v232, v242, -v70
	v_mfma_f32_32x32x16_f16 v[206:221], v[54:57], v[90:93], v[206:221]
	v_fma_f32 v72, v232, v243, v72
	v_fma_f32 v71, v232, v244, -v71
	v_fma_f32 v73, v232, v245, v73
	v_cvt_pk_f16_f32 v247, v70, v71
	v_cvt_pk_f16_f32 v249, v72, v73
	v_mfma_f32_32x32x16_f16 v[34:49], v[2:5], v[150:153], 0
	v_mul_f32_e32 v66, v235, v239
	v_mul_f32_e32 v68, v235, v238
	v_mul_f32_e32 v67, v235, v241
	v_mul_f32_e32 v69, v235, v240
	v_fma_f32 v66, v234, v238, -v66
	v_mfma_f32_32x32x16_f16 v[34:49], v[18:21], v[146:149], v[34:49]
	v_fma_f32 v68, v234, v239, v68
	v_fma_f32 v67, v234, v240, -v67
	v_fma_f32 v69, v234, v241, v69
	v_cvt_pk_f16_f32 v250, v66, v67
	v_cvt_pk_f16_f32 v252, v68, v69
	v_mfma_f32_32x32x16_f16 v[34:49], v[6:9], v[142:145], v[34:49]
	v_mul_f32_e32 v70, v237, v243
	v_mul_f32_e32 v72, v237, v242
	v_mul_f32_e32 v71, v237, v245
	v_mul_f32_e32 v73, v237, v244
	v_fma_f32 v70, v236, v242, -v70
	v_mfma_f32_32x32x16_f16 v[34:49], v[22:25], v[138:141], v[34:49]
	v_fma_f32 v72, v236, v243, v72
	v_fma_f32 v71, v236, v244, -v71
	v_fma_f32 v73, v236, v245, v73
	v_cvt_pk_f16_f32 v251, v70, v71
	v_cvt_pk_f16_f32 v253, v72, v73
	v_mfma_f32_32x32x16_f16 v[50:65], v[2:5], v[134:137], 0
	v_cvt_pk_f16_f32 v190, v190, v191
	v_cvt_pk_f16_f32 v191, v192, v193
	v_cvt_pk_f16_f32 v192, v194, v195
	v_cvt_pk_f16_f32 v193, v196, v197
	v_cvt_pk_f16_f32 v194, v198, v199
	v_mfma_f32_32x32x16_f16 v[50:65], v[18:21], v[126:129], v[50:65]
	v_cvt_pk_f16_f32 v195, v200, v201
	v_cvt_pk_f16_f32 v196, v202, v203
	v_cvt_pk_f16_f32 v197, v204, v205
	v_cvt_pk_f16_f32 v206, v206, v207
	v_cvt_pk_f16_f32 v207, v208, v209
	v_mfma_f32_32x32x16_f16 v[50:65], v[6:9], v[122:125], v[50:65]
	v_cvt_pk_f16_f32 v208, v210, v211
	v_cvt_pk_f16_f32 v209, v212, v213
	v_cvt_pk_f16_f32 v210, v214, v215
	v_cvt_pk_f16_f32 v211, v216, v217
	v_cvt_pk_f16_f32 v212, v218, v219
	v_mfma_f32_32x32x16_f16 v[50:65], v[22:25], v[130:133], v[50:65]
	v_cvt_pk_f16_f32 v213, v220, v221
	ds_write_b128 v173, v[190:193]
	ds_write_b128 v172, v[194:197]
	ds_write_b128 v173, v[206:209] offset:32768
	ds_write_b128 v172, v[210:213] offset:32768
	v_xor_b32_e32 v255, 24, v254
	ds_read2_b64 v[238:241], v255 offset0:0 offset1:16
	ds_read2_b64 v[242:245], v255 offset0:32 offset1:48
	v_mfma_f32_32x32x16_f16 v[2:17], v[222:225], v[246:249], 0
	v_mfma_f32_32x32x16_f16 v[18:33], v[226:229], v[250:253], 0
	v_cvt_pk_f16_f32 v34, v34, v35
	v_cvt_pk_f16_f32 v35, v36, v37
	v_cvt_pk_f16_f32 v36, v38, v39
	v_cvt_pk_f16_f32 v37, v40, v41
	v_cvt_pk_f16_f32 v38, v42, v43
	v_cvt_pk_f16_f32 v39, v44, v45
	v_cvt_pk_f16_f32 v40, v46, v47
	v_cvt_pk_f16_f32 v41, v48, v49
	v_cvt_pk_f16_f32 v50, v50, v51
	v_cvt_pk_f16_f32 v51, v52, v53
	v_cvt_pk_f16_f32 v52, v54, v55
	v_cvt_pk_f16_f32 v53, v56, v57
	v_cvt_pk_f16_f32 v54, v58, v59
	v_cvt_pk_f16_f32 v55, v60, v61
	v_cvt_pk_f16_f32 v56, v62, v63
	v_cvt_pk_f16_f32 v57, v64, v65
	v_mfma_f32_32x32x16_f16 v[190:205], v[34:37], v[118:121], 0
	v_cvt_pk_f16_f32 v2, v2, v3
	v_cvt_pk_f16_f32 v3, v4, v5
	v_cvt_pk_f16_f32 v4, v6, v7
	v_cvt_pk_f16_f32 v5, v8, v9
	v_mfma_f32_32x32x16_f16 v[206:221], v[34:37], v[102:105], 0
	v_cvt_pk_f16_f32 v6, v10, v11
	v_cvt_pk_f16_f32 v7, v12, v13
	v_cvt_pk_f16_f32 v8, v14, v15
	v_cvt_pk_f16_f32 v9, v16, v17
	v_cvt_pk_f16_f32 v18, v18, v19
	v_mfma_f32_32x32x16_f16 v[190:205], v[38:41], v[114:117], v[190:205]
	v_cvt_pk_f16_f32 v19, v20, v21
	v_cvt_pk_f16_f32 v20, v22, v23
	v_cvt_pk_f16_f32 v21, v24, v25
	v_cvt_pk_f16_f32 v22, v26, v27
	v_mfma_f32_32x32x16_f16 v[206:221], v[38:41], v[98:101], v[206:221]
	v_cvt_pk_f16_f32 v23, v28, v29
	v_cvt_pk_f16_f32 v24, v30, v31
	v_cvt_pk_f16_f32 v25, v32, v33
	s_waitcnt lgkmcnt(0)
	v_mul_f32_e32 v66, v231, v239
	v_mfma_f32_32x32x16_f16 v[190:205], v[50:53], v[110:113], v[190:205]
	v_mul_f32_e32 v68, v231, v238
	v_mul_f32_e32 v67, v231, v241
	v_mul_f32_e32 v69, v231, v240
	v_fma_f32 v66, v230, v238, -v66
	v_fma_f32 v68, v230, v239, v68
	v_mfma_f32_32x32x16_f16 v[206:221], v[50:53], v[94:97], v[206:221]
	v_fma_f32 v67, v230, v240, -v67
	v_fma_f32 v69, v230, v241, v69
	v_cvt_pk_f16_f32 v246, v66, v67
	v_cvt_pk_f16_f32 v248, v68, v69
	v_mfma_f32_32x32x16_f16 v[190:205], v[54:57], v[106:109], v[190:205]
	v_mul_f32_e32 v70, v233, v243
	v_mul_f32_e32 v72, v233, v242
	v_mul_f32_e32 v71, v233, v245
	v_mul_f32_e32 v73, v233, v244
	v_fma_f32 v70, v232, v242, -v70
	v_mfma_f32_32x32x16_f16 v[206:221], v[54:57], v[90:93], v[206:221]
	v_fma_f32 v72, v232, v243, v72
	v_fma_f32 v71, v232, v244, -v71
	v_fma_f32 v73, v232, v245, v73
	v_cvt_pk_f16_f32 v247, v70, v71
	v_cvt_pk_f16_f32 v249, v72, v73
	v_mfma_f32_32x32x16_f16 v[34:49], v[2:5], v[150:153], 0
	v_mul_f32_e32 v66, v235, v239
	v_mul_f32_e32 v68, v235, v238
	v_mul_f32_e32 v67, v235, v241
	v_mul_f32_e32 v69, v235, v240
	v_fma_f32 v66, v234, v238, -v66
	v_mfma_f32_32x32x16_f16 v[34:49], v[18:21], v[146:149], v[34:49]
	v_fma_f32 v68, v234, v239, v68
	v_fma_f32 v67, v234, v240, -v67
	v_fma_f32 v69, v234, v241, v69
	v_cvt_pk_f16_f32 v250, v66, v67
	v_cvt_pk_f16_f32 v252, v68, v69
	v_mfma_f32_32x32x16_f16 v[34:49], v[6:9], v[142:145], v[34:49]
	v_mul_f32_e32 v70, v237, v243
	v_mul_f32_e32 v72, v237, v242
	v_mul_f32_e32 v71, v237, v245
	v_mul_f32_e32 v73, v237, v244
	v_fma_f32 v70, v236, v242, -v70
	v_mfma_f32_32x32x16_f16 v[34:49], v[22:25], v[138:141], v[34:49]
	v_fma_f32 v72, v236, v243, v72
	v_fma_f32 v71, v236, v244, -v71
	v_fma_f32 v73, v236, v245, v73
	v_cvt_pk_f16_f32 v251, v70, v71
	v_cvt_pk_f16_f32 v253, v72, v73
	v_cvt_pk_f16_f32 v190, v190, v191
	v_mfma_f32_32x32x16_f16 v[50:65], v[2:5], v[134:137], 0
	v_cvt_pk_f16_f32 v191, v192, v193
	v_cvt_pk_f16_f32 v192, v194, v195
	v_cvt_pk_f16_f32 v193, v196, v197
	v_cvt_pk_f16_f32 v194, v198, v199
	v_cvt_pk_f16_f32 v195, v200, v201
	v_mfma_f32_32x32x16_f16 v[50:65], v[18:21], v[126:129], v[50:65]
	v_cvt_pk_f16_f32 v196, v202, v203
	v_cvt_pk_f16_f32 v197, v204, v205
	v_cvt_pk_f16_f32 v206, v206, v207
	v_cvt_pk_f16_f32 v207, v208, v209
	v_cvt_pk_f16_f32 v208, v210, v211
	v_mfma_f32_32x32x16_f16 v[50:65], v[6:9], v[122:125], v[50:65]
	v_cvt_pk_f16_f32 v209, v212, v213
	v_cvt_pk_f16_f32 v210, v214, v215
	v_cvt_pk_f16_f32 v211, v216, v217
	v_cvt_pk_f16_f32 v212, v218, v219
	v_cvt_pk_f16_f32 v213, v220, v221
	v_mfma_f32_32x32x16_f16 v[50:65], v[22:25], v[130:133], v[50:65]
	v_xor_b32_e32 v74, 0x8a0, v173
	v_xor_b32_e32 v75, 0x8a0, v172
	ds_write_b128 v74, v[190:193]
	ds_write_b128 v75, v[194:197]
	ds_write_b128 v74, v[206:209] offset:32768
	ds_write_b128 v75, v[210:213] offset:32768
	s_nop 0
	v_mfma_f32_32x32x16_f16 v[2:17], v[222:225], v[246:249], 0
	v_mfma_f32_32x32x16_f16 v[18:33], v[226:229], v[250:253], 0
	v_cvt_pk_f16_f32 v34, v34, v35
	v_cvt_pk_f16_f32 v35, v36, v37
	v_cvt_pk_f16_f32 v36, v38, v39
	v_cvt_pk_f16_f32 v37, v40, v41
	v_cvt_pk_f16_f32 v38, v42, v43
	v_cvt_pk_f16_f32 v39, v44, v45
	v_cvt_pk_f16_f32 v40, v46, v47
	v_cvt_pk_f16_f32 v41, v48, v49
	v_cvt_pk_f16_f32 v50, v50, v51
	v_cvt_pk_f16_f32 v51, v52, v53
	v_cvt_pk_f16_f32 v52, v54, v55
	v_cvt_pk_f16_f32 v53, v56, v57
	v_cvt_pk_f16_f32 v54, v58, v59
	v_cvt_pk_f16_f32 v55, v60, v61
	v_cvt_pk_f16_f32 v56, v62, v63
	v_cvt_pk_f16_f32 v57, v64, v65
	v_mfma_f32_32x32x16_f16 v[190:205], v[34:37], v[118:121], 0
	v_cvt_pk_f16_f32 v2, v2, v3
	v_cvt_pk_f16_f32 v3, v4, v5
	v_mfma_f32_32x32x16_f16 v[206:221], v[34:37], v[102:105], 0
	v_cvt_pk_f16_f32 v4, v6, v7
	v_cvt_pk_f16_f32 v5, v8, v9
	v_mfma_f32_32x32x16_f16 v[190:205], v[38:41], v[114:117], v[190:205]
	v_cvt_pk_f16_f32 v6, v10, v11
	v_cvt_pk_f16_f32 v7, v12, v13
	v_mfma_f32_32x32x16_f16 v[206:221], v[38:41], v[98:101], v[206:221]
	v_cvt_pk_f16_f32 v8, v14, v15
	v_cvt_pk_f16_f32 v9, v16, v17
	v_mfma_f32_32x32x16_f16 v[190:205], v[50:53], v[110:113], v[190:205]
	v_cvt_pk_f16_f32 v18, v18, v19
	v_cvt_pk_f16_f32 v19, v20, v21
	v_mfma_f32_32x32x16_f16 v[206:221], v[50:53], v[94:97], v[206:221]
	v_cvt_pk_f16_f32 v20, v22, v23
	v_cvt_pk_f16_f32 v21, v24, v25
	v_mfma_f32_32x32x16_f16 v[190:205], v[54:57], v[106:109], v[190:205]
	v_cvt_pk_f16_f32 v22, v26, v27
	v_cvt_pk_f16_f32 v23, v28, v29
	v_mfma_f32_32x32x16_f16 v[206:221], v[54:57], v[90:93], v[206:221]
	v_cvt_pk_f16_f32 v24, v30, v31
	v_cvt_pk_f16_f32 v25, v32, v33
	v_mfma_f32_32x32x16_f16 v[34:49], v[2:5], v[150:153], 0
	v_mfma_f32_32x32x16_f16 v[34:49], v[18:21], v[146:149], v[34:49]
	v_mfma_f32_32x32x16_f16 v[34:49], v[6:9], v[142:145], v[34:49]
	v_mfma_f32_32x32x16_f16 v[34:49], v[22:25], v[138:141], v[34:49]
	v_mfma_f32_32x32x16_f16 v[50:65], v[2:5], v[134:137], 0
	s_nop 5
	v_cvt_pk_f16_f32 v190, v190, v191
	v_cvt_pk_f16_f32 v191, v192, v193
	v_cvt_pk_f16_f32 v192, v194, v195
	v_cvt_pk_f16_f32 v193, v196, v197
	v_mfma_f32_32x32x16_f16 v[50:65], v[18:21], v[126:129], v[50:65]
	v_cvt_pk_f16_f32 v194, v198, v199
	v_cvt_pk_f16_f32 v195, v200, v201
	v_cvt_pk_f16_f32 v196, v202, v203
	v_cvt_pk_f16_f32 v197, v204, v205
	v_cvt_pk_f16_f32 v206, v206, v207
	v_cvt_pk_f16_f32 v207, v208, v209
	v_mfma_f32_32x32x16_f16 v[50:65], v[6:9], v[122:125], v[50:65]
	v_cvt_pk_f16_f32 v208, v210, v211
	v_cvt_pk_f16_f32 v209, v212, v213
	v_cvt_pk_f16_f32 v210, v214, v215
	v_cvt_pk_f16_f32 v211, v216, v217
	v_cvt_pk_f16_f32 v212, v218, v219
	v_cvt_pk_f16_f32 v213, v220, v221
	v_mfma_f32_32x32x16_f16 v[50:65], v[22:25], v[130:133], v[50:65]
	v_xor_b32_e32 v74, 0x1040, v173
	v_xor_b32_e32 v75, 0x1040, v172
	ds_write_b128 v74, v[190:193]
	ds_write_b128 v75, v[194:197]
	ds_write_b128 v74, v[206:209] offset:32768
	ds_write_b128 v75, v[210:213] offset:32768
	s_nop 11
	v_cvt_pk_f16_f32 v34, v34, v35
	v_cvt_pk_f16_f32 v35, v36, v37
	v_cvt_pk_f16_f32 v36, v38, v39
	v_cvt_pk_f16_f32 v37, v40, v41
	v_cvt_pk_f16_f32 v38, v42, v43
	v_cvt_pk_f16_f32 v39, v44, v45
	v_cvt_pk_f16_f32 v40, v46, v47
	v_cvt_pk_f16_f32 v41, v48, v49
	v_cvt_pk_f16_f32 v50, v50, v51
	v_cvt_pk_f16_f32 v51, v52, v53
	v_cvt_pk_f16_f32 v52, v54, v55
	v_cvt_pk_f16_f32 v53, v56, v57
	v_cvt_pk_f16_f32 v54, v58, v59
	v_cvt_pk_f16_f32 v55, v60, v61
	v_cvt_pk_f16_f32 v56, v62, v63
	v_cvt_pk_f16_f32 v57, v64, v65
	v_mfma_f32_32x32x16_f16 v[190:205], v[34:37], v[118:121], 0
	v_mfma_f32_32x32x16_f16 v[206:221], v[34:37], v[102:105], 0
	v_mfma_f32_32x32x16_f16 v[190:205], v[38:41], v[114:117], v[190:205]
	v_mfma_f32_32x32x16_f16 v[206:221], v[38:41], v[98:101], v[206:221]
	v_mfma_f32_32x32x16_f16 v[190:205], v[50:53], v[110:113], v[190:205]
	v_mfma_f32_32x32x16_f16 v[206:221], v[50:53], v[94:97], v[206:221]
	v_mfma_f32_32x32x16_f16 v[190:205], v[54:57], v[106:109], v[190:205]
	v_mfma_f32_32x32x16_f16 v[206:221], v[54:57], v[90:93], v[206:221]
	v_and_b32_e32 v134, 1, v156
	v_bitop3_b32 v132, v171, s40, v170 bitop3:0x36
	v_bitop3_b32 v131, s41, v154, v160 bitop3:0x36
	v_bitop3_b32 v135, v171, s42, v170 bitop3:0x36
	v_xor_b32_e32 v133, s43, v154
	v_and_b32_e32 v130, 4, v156
	s_lshl_b32 s2, s27, 3
	s_lshl_b32 s3, s5, 2
	s_or_b32 s2, s3, s2
	s_ashr_i32 s3, s2, 31
	s_lshl_b64 s[2:3], s[2:3], 13
	s_add_u32 s2, s20, s2
	s_addc_u32 s3, s21, s3
	v_lshlrev_b32_e32 v154, 1, v169
	v_lshl_add_u64 v[2:3], s[2:3], 0, v[154:155]
	v_add_co_u32_e32 v2, vcc, s23, v2
	s_nop 1
	v_addc_co_u32_e32 v3, vcc, 0, v3, vcc
	v_cvt_pk_f16_f32 v190, v190, v191
	v_cvt_pk_f16_f32 v191, v192, v193
	v_cvt_pk_f16_f32 v192, v194, v195
	v_cvt_pk_f16_f32 v193, v196, v197
	v_cvt_pk_f16_f32 v194, v198, v199
	v_cvt_pk_f16_f32 v195, v200, v201
	v_cvt_pk_f16_f32 v196, v202, v203
	v_cvt_pk_f16_f32 v197, v204, v205
	v_cvt_pk_f16_f32 v206, v206, v207
	v_cvt_pk_f16_f32 v207, v208, v209
	v_cvt_pk_f16_f32 v208, v210, v211
	v_cvt_pk_f16_f32 v209, v212, v213
	v_cvt_pk_f16_f32 v210, v214, v215
	v_cvt_pk_f16_f32 v211, v216, v217
	v_cvt_pk_f16_f32 v212, v218, v219
	v_cvt_pk_f16_f32 v213, v220, v221
	v_xor_b32_e32 v74, 0x18e0, v173
	v_xor_b32_e32 v75, 0x18e0, v172
	ds_write_b128 v74, v[190:193]
	ds_write_b128 v75, v[194:197]
	ds_write_b128 v74, v[206:209] offset:32768
	ds_write_b128 v75, v[210:213] offset:32768
	s_setprio 0
	s_waitcnt lgkmcnt(0)
	s_barrier
	global_load_dwordx4 v[62:65], v154, s[2:3]
	global_load_dwordx4 v[46:49], v154, s[2:3] offset:1024
	global_load_dwordx4 v[42:45], v154, s[2:3] offset:2048
	global_load_dwordx4 v[38:41], v154, s[2:3] offset:3072
	global_load_dwordx4 v[54:57], v[2:3], off offset:1024
	global_load_dwordx4 v[50:53], v[2:3], off offset:2048
	v_lshl_add_u64 v[4:5], s[12:13], 0, v[154:155]
	global_load_dwordx4 v[126:129], v154, s[12:13]
	global_load_dwordx4 v[122:125], v154, s[12:13] offset:1024
	global_load_dwordx4 v[118:121], v154, s[12:13] offset:2048
	global_load_dwordx4 v[114:117], v154, s[12:13] offset:3072
	global_load_dwordx4 v[34:37], v168, s[2:3]
	global_load_dwordx4 v[110:113], v168, s[12:13]
	v_add_co_u32_e32 v4, vcc, s23, v4
	s_nop 1
	v_addc_co_u32_e32 v5, vcc, 0, v5, vcc
	global_load_dwordx4 v[58:61], v[2:3], off offset:3072
	global_load_dwordx4 v[106:109], v[4:5], off offset:1024
	global_load_dwordx4 v[94:97], v[4:5], off offset:2048
	global_load_dwordx4 v[90:93], v[4:5], off offset:3072
	v_bfrev_b32_e32 v3, v156
	v_lshlrev_b32_e32 v7, 5, v167
	v_lshlrev_b32_e32 v6, 9, v167
	v_and_b32_e32 v7, 0x200, v7
	v_lshlrev_b32_e32 v8, 8, v167
	v_lshrrev_b32_e32 v3, 27, v3
	v_lshrrev_b32_e32 v2, 2, v167
	v_lshrrev_b32_e32 v4, 4, v156
	v_xor_b32_e32 v5, v169, v156
	v_and_b32_e32 v6, 0x5800, v6
	v_and_b32_e32 v3, 8, v3
	v_and_or_b32 v7, v8, s24, v7
	v_lshrrev_b32_e32 v5, 1, v5
	v_xor_b32_e32 v4, v2, v4
	v_or3_b32 v3, v7, v6, v3
	v_bitop3_b32 v7, v2, v182, 1 bitop3:0x6c
	v_lshlrev_b32_e32 v2, 1, v167
	v_and_b32_e32 v5, 4, v5
	v_lshlrev_b32_e32 v4, 3, v4
	v_lshrrev_b32_e32 v6, 1, v167
	v_and_b32_e32 v2, 2, v2
	v_and_or_b32 v9, v169, 8, v2
	v_and_b32_e32 v2, 8, v4
	v_and_or_b32 v4, v6, 2, v5
	v_or3_b32 v2, v4, v2, v134
	v_lshlrev_b32_e32 v2, 4, v2
	v_bitop3_b32 v146, v3, s28, v2 bitop3:0x36
	v_xor_b32_e32 v8, v6, v182
	v_xor_b32_e32 v147, 0x2010, v146
	v_lshlrev_b32_e32 v8, 2, v8
	v_and_b32_e32 v8, 4, v8
	v_or3_b32 v6, v9, v7, v8
	v_lshlrev_b32_e32 v7, 11, v167
	v_and_b32_e32 v8, 0x7800, v7
	v_lshlrev_b32_e32 v6, 4, v6
	v_or3_b32 v22, v6, v8, v170
	v_and_b32_e32 v23, 0x8000, v7
	v_xor_b32_e32 v150, 16, v146
	v_xad_u32 v70, v22, s28, v23
	v_xor_b32_e32 v151, 0x2000, v146
	ds_read_b64_tr_b16 v[18:19], v146
	ds_read_b64_tr_b16 v[20:21], v147
	ds_read_b64_tr_b16 v[22:23], v146 offset:32768
	ds_read_b64_tr_b16 v[24:25], v147 offset:32768
	ds_read_b64_tr_b16 v[26:27], v150
	ds_read_b64_tr_b16 v[28:29], v151
	ds_read_b64_tr_b16 v[30:31], v150 offset:32768
	ds_read_b64_tr_b16 v[32:33], v151 offset:32768
	v_xor_b32_e32 v148, 32, v146
	v_xor_b32_e32 v149, 0x2030, v146
	v_xor_b32_e32 v144, 48, v146
	v_xor_b32_e32 v145, 0x2020, v146
	v_xor_b32_e32 v142, 64, v146
	v_xor_b32_e32 v143, 0x2050, v146
	v_xor_b32_e32 v140, 0x50, v146
	v_xor_b32_e32 v141, 0x2040, v146
	v_xor_b32_e32 v138, 0x60, v146
	v_xor_b32_e32 v139, 0x2070, v146
	v_xor_b32_e32 v136, 0x70, v146
	v_xor_b32_e32 v137, 0x2060, v146
	v_xor_b32_e32 v71, 0x60, v70
	s_lshl_b64 s[0:1], s[0:1], 13
	s_add_u32 s0, s8, s0
	s_addc_u32 s1, s9, s1
	s_waitcnt vmcnt(17) lgkmcnt(4)
	v_mfma_f32_32x32x16_f16 v[2:17], v[18:21], v[86:89], 0
	s_waitcnt vmcnt(16)
	v_mfma_f32_32x32x16_f16 v[2:17], v[22:25], v[82:85], v[2:17]
	ds_read_b64_tr_b16 v[206:207], v148
	ds_read_b64_tr_b16 v[208:209], v149
	ds_read_b64_tr_b16 v[210:211], v148 offset:32768
	ds_read_b64_tr_b16 v[212:213], v149 offset:32768
	s_waitcnt lgkmcnt(4)
	v_mfma_f32_32x32x16_f16 v[190:205], v[26:29], v[86:89], 0
	v_mfma_f32_32x32x16_f16 v[190:205], v[30:33], v[82:85], v[190:205]
	s_nop 4
	v_cvt_pk_f16_f32 v2, v2, v3
	v_cvt_pk_f16_f32 v3, v4, v5
	v_cvt_pk_f16_f32 v4, v6, v7
	v_cvt_pk_f16_f32 v5, v8, v9
	v_cvt_pk_f16_f32 v6, v10, v11
	v_cvt_pk_f16_f32 v7, v12, v13
	v_cvt_pk_f16_f32 v8, v14, v15
	v_cvt_pk_f16_f32 v9, v16, v17
	v_xor_b32_e32 v73, 0x280, v70
	ds_write_b128 v70, v[2:5]
	ds_write_b128 v73, v[6:9]
	ds_read_b64_tr_b16 v[18:19], v144
	ds_read_b64_tr_b16 v[20:21], v145
	ds_read_b64_tr_b16 v[22:23], v144 offset:32768
	ds_read_b64_tr_b16 v[24:25], v145 offset:32768
	s_waitcnt lgkmcnt(6)
	v_mfma_f32_32x32x16_f16 v[2:17], v[206:209], v[86:89], 0
	v_mfma_f32_32x32x16_f16 v[2:17], v[210:213], v[82:85], v[2:17]
	v_cvt_pk_f16_f32 v190, v190, v191
	v_cvt_pk_f16_f32 v191, v192, v193
	v_cvt_pk_f16_f32 v192, v194, v195
	v_cvt_pk_f16_f32 v193, v196, v197
	v_cvt_pk_f16_f32 v194, v198, v199
	v_cvt_pk_f16_f32 v195, v200, v201
	v_cvt_pk_f16_f32 v196, v202, v203
	v_cvt_pk_f16_f32 v197, v204, v205
	v_xor_b32_e32 v72, 16, v70
	v_xor_b32_e32 v73, 0x290, v70
	ds_write_b128 v72, v[190:193]
	ds_write_b128 v73, v[194:197]
	ds_read_b64_tr_b16 v[26:27], v142
	ds_read_b64_tr_b16 v[28:29], v143
	ds_read_b64_tr_b16 v[30:31], v142 offset:32768
	ds_read_b64_tr_b16 v[32:33], v143 offset:32768
	s_waitcnt lgkmcnt(6)
	v_mfma_f32_32x32x16_f16 v[190:205], v[18:21], v[86:89], 0
	v_mfma_f32_32x32x16_f16 v[190:205], v[22:25], v[82:85], v[190:205]
	v_cvt_pk_f16_f32 v2, v2, v3
	v_cvt_pk_f16_f32 v3, v4, v5
	v_cvt_pk_f16_f32 v4, v6, v7
	v_cvt_pk_f16_f32 v5, v8, v9
	v_cvt_pk_f16_f32 v6, v10, v11
	v_cvt_pk_f16_f32 v7, v12, v13
	v_cvt_pk_f16_f32 v8, v14, v15
	v_cvt_pk_f16_f32 v9, v16, v17
	v_xor_b32_e32 v72, 32, v70
	v_xor_b32_e32 v73, 0x2a0, v70
	ds_write_b128 v72, v[2:5]
	ds_write_b128 v73, v[6:9]
	ds_read_b64_tr_b16 v[206:207], v140
	ds_read_b64_tr_b16 v[208:209], v141
	ds_read_b64_tr_b16 v[210:211], v140 offset:32768
	ds_read_b64_tr_b16 v[212:213], v141 offset:32768
	s_waitcnt lgkmcnt(6)
	v_mfma_f32_32x32x16_f16 v[2:17], v[26:29], v[86:89], 0
	v_mfma_f32_32x32x16_f16 v[2:17], v[30:33], v[82:85], v[2:17]
	v_cvt_pk_f16_f32 v190, v190, v191
	v_cvt_pk_f16_f32 v191, v192, v193
	v_cvt_pk_f16_f32 v192, v194, v195
	v_cvt_pk_f16_f32 v193, v196, v197
	v_cvt_pk_f16_f32 v194, v198, v199
	v_cvt_pk_f16_f32 v195, v200, v201
	v_cvt_pk_f16_f32 v196, v202, v203
	v_cvt_pk_f16_f32 v197, v204, v205
	v_xor_b32_e32 v72, 48, v70
	v_xor_b32_e32 v73, 0x2b0, v70
	ds_write_b128 v72, v[190:193]
	ds_write_b128 v73, v[194:197]
	ds_read_b64_tr_b16 v[18:19], v138
	ds_read_b64_tr_b16 v[20:21], v139
	ds_read_b64_tr_b16 v[22:23], v138 offset:32768
	ds_read_b64_tr_b16 v[24:25], v139 offset:32768
	s_waitcnt lgkmcnt(6)
	v_mfma_f32_32x32x16_f16 v[190:205], v[206:209], v[86:89], 0
	v_mfma_f32_32x32x16_f16 v[190:205], v[210:213], v[82:85], v[190:205]
	v_cvt_pk_f16_f32 v2, v2, v3
	v_cvt_pk_f16_f32 v3, v4, v5
	v_cvt_pk_f16_f32 v4, v6, v7
	v_cvt_pk_f16_f32 v5, v8, v9
	v_cvt_pk_f16_f32 v6, v10, v11
	v_cvt_pk_f16_f32 v7, v12, v13
	v_cvt_pk_f16_f32 v8, v14, v15
	v_cvt_pk_f16_f32 v9, v16, v17
	v_xor_b32_e32 v72, 64, v70
	v_xor_b32_e32 v73, 0x2c0, v70
	ds_write_b128 v72, v[2:5]
	ds_write_b128 v73, v[6:9]
	ds_read_b64_tr_b16 v[26:27], v136
	ds_read_b64_tr_b16 v[28:29], v137
	ds_read_b64_tr_b16 v[30:31], v136 offset:32768
	ds_read_b64_tr_b16 v[32:33], v137 offset:32768
	s_waitcnt lgkmcnt(6)
	v_mfma_f32_32x32x16_f16 v[2:17], v[18:21], v[86:89], 0
	v_mfma_f32_32x32x16_f16 v[2:17], v[22:25], v[82:85], v[2:17]
	v_cvt_pk_f16_f32 v190, v190, v191
	v_cvt_pk_f16_f32 v191, v192, v193
	v_cvt_pk_f16_f32 v192, v194, v195
	v_cvt_pk_f16_f32 v193, v196, v197
	v_cvt_pk_f16_f32 v194, v198, v199
	v_cvt_pk_f16_f32 v195, v200, v201
	v_cvt_pk_f16_f32 v196, v202, v203
	v_cvt_pk_f16_f32 v197, v204, v205
	v_xor_b32_e32 v72, 0x50, v70
	v_xor_b32_e32 v73, 0x2d0, v70
	ds_write_b128 v72, v[190:193]
	ds_write_b128 v73, v[194:197]
	s_waitcnt lgkmcnt(2)
	v_mfma_f32_32x32x16_f16 v[190:205], v[26:29], v[86:89], 0
	v_mfma_f32_32x32x16_f16 v[190:205], v[30:33], v[82:85], v[190:205]
	v_cvt_pk_f16_f32 v2, v2, v3
	v_cvt_pk_f16_f32 v3, v4, v5
	v_cvt_pk_f16_f32 v4, v6, v7
	v_cvt_pk_f16_f32 v5, v8, v9
	v_cvt_pk_f16_f32 v6, v10, v11
	v_cvt_pk_f16_f32 v7, v12, v13
	v_cvt_pk_f16_f32 v8, v14, v15
	v_cvt_pk_f16_f32 v9, v16, v17
	v_xor_b32_e32 v72, 0x60, v70
	v_xor_b32_e32 v73, 0x2e0, v70
	ds_write_b128 v72, v[2:5]
	ds_write_b128 v73, v[6:9]
	v_cvt_pk_f16_f32 v190, v190, v191
	v_cvt_pk_f16_f32 v191, v192, v193
	v_cvt_pk_f16_f32 v192, v194, v195
	v_cvt_pk_f16_f32 v193, v196, v197
	v_cvt_pk_f16_f32 v194, v198, v199
	v_cvt_pk_f16_f32 v195, v200, v201
	v_cvt_pk_f16_f32 v196, v202, v203
	v_cvt_pk_f16_f32 v197, v204, v205
	v_xor_b32_e32 v72, 0x70, v70
	v_xor_b32_e32 v73, 0x2f0, v70
	ds_write_b128 v72, v[190:193]
	ds_write_b128 v73, v[194:197]
	v_lshl_add_u64 v[2:3], s[0:1], 0, v[154:155]
	v_lshl_add_u64 v[4:5], v[2:3], 0, s[18:19]
	v_add_co_u32_e32 v2, vcc, s25, v2
	s_waitcnt lgkmcnt(0)
	s_nop 0
	v_addc_co_u32_e32 v3, vcc, 0, v3, vcc
	s_barrier
	s_nop 0
	s_nop 0
	global_load_dwordx4 v[102:105], v[2:3], off
	global_load_dwordx4 v[98:101], v[4:5], off offset:1024
	s_setprio 1
	s_add_u32 s0, s2, 0x2000
	s_addc_u32 s1, s3, 0
	v_lshl_add_u64 v[2:3], s[0:1], 0, v[154:155]
	v_add_co_u32_e32 v2, vcc, s23, v2
	global_load_dwordx4 v[66:69], v154, s[0:1]
	global_load_dwordx4 v[70:73], v154, s[0:1] offset:1024
	global_load_dwordx4 v[74:77], v154, s[0:1] offset:2048
	global_load_dwordx4 v[78:81], v154, s[0:1] offset:3072
	v_addc_co_u32_e32 v3, vcc, 0, v3, vcc
	global_load_dwordx4 v[82:85], v168, s[0:1]
	global_load_dwordx4 v[86:89], v[2:3], off offset:1024
	global_load_dwordx4 v[182:185], v[2:3], off offset:2048
	global_load_dwordx4 v[186:189], v[2:3], off offset:3072
	ds_read_b128 v[18:21], v179
	ds_read_b128 v[22:25], v179 offset:32768
	ds_read_b128 v[26:29], v178
	ds_read_b128 v[30:33], v178 offset:32768
	s_add_u32 s0, s2, 0x6000
	s_addc_u32 s1, s3, 0
	s_waitcnt vmcnt(25) lgkmcnt(3)
	v_mfma_f32_32x32x16_f16 v[2:17], v[18:21], v[62:65], 0
	s_add_u32 s2, s2, 0x4000
	s_addc_u32 s3, s3, 0
	s_or_b32 s27, s26, 0x8a0
	s_or_b32 s26, s26, 0xa20
	s_waitcnt vmcnt(24) lgkmcnt(1)
	v_mfma_f32_32x32x16_f16 v[2:17], v[26:29], v[46:49], v[2:17]
	s_waitcnt vmcnt(23)
	v_mfma_f32_32x32x16_f16 v[2:17], v[22:25], v[42:45], v[2:17]
	s_waitcnt vmcnt(22) lgkmcnt(0)
	v_mfma_f32_32x32x16_f16 v[2:17], v[30:33], v[38:41], v[2:17]
	s_waitcnt vmcnt(15)
	v_mfma_f32_32x32x16_f16 v[34:49], v[18:21], v[34:37], 0
	s_nop 9
	v_cvt_pk_f16_f32 v9, v8, v9
	v_cvt_pk_f16_f32 v8, v6, v7
	v_cvt_pk_f16_f32 v7, v4, v5
	v_cvt_pk_f16_f32 v6, v2, v3
	v_cvt_pk_f16_f32 v5, v16, v17
	v_cvt_pk_f16_f32 v4, v14, v15
	v_cvt_pk_f16_f32 v3, v12, v13
	v_mfma_f32_32x32x16_f16 v[34:49], v[26:29], v[54:57], v[34:49]
	v_cvt_pk_f16_f32 v2, v10, v11
	v_mfma_f32_32x32x16_f16 v[34:49], v[22:25], v[50:53], v[34:49]
	s_waitcnt vmcnt(13)
	v_mfma_f32_32x32x16_f16 v[34:49], v[30:33], v[58:61], v[34:49]
	v_mfma_f32_32x32x16_f16 v[18:33], v[6:9], v[126:129], 0
	s_nop 10
	v_cvt_pk_f16_f32 v13, v40, v41
	v_cvt_pk_f16_f32 v12, v38, v39
	v_cvt_pk_f16_f32 v11, v36, v37
	v_cvt_pk_f16_f32 v10, v34, v35
	v_cvt_pk_f16_f32 v17, v48, v49
	v_cvt_pk_f16_f32 v16, v46, v47
	v_cvt_pk_f16_f32 v15, v44, v45
	v_mfma_f32_32x32x16_f16 v[50:65], v[6:9], v[110:113], 0
	v_bitop3_b32 v6, v171, s27, v170 bitop3:0x36
	v_cvt_pk_f16_f32 v14, v42, v43
	v_mfma_f32_32x32x16_f16 v[18:33], v[2:5], v[122:125], v[18:33]
	s_waitcnt vmcnt(12)
	v_mfma_f32_32x32x16_f16 v[50:65], v[2:5], v[106:109], v[50:65]
	ds_read_b128 v[2:5], v6
	ds_read_b128 v[6:9], v6 offset:32768
	v_mfma_f32_32x32x16_f16 v[18:33], v[10:13], v[118:121], v[18:33]
	s_waitcnt vmcnt(11)
	v_mfma_f32_32x32x16_f16 v[50:65], v[10:13], v[94:97], v[50:65]
	s_waitcnt vmcnt(7) lgkmcnt(1)
	v_mfma_f32_32x32x16_f16 v[34:49], v[2:5], v[66:69], 0
	v_mfma_f32_32x32x16_f16 v[18:33], v[14:17], v[114:117], v[18:33]
	v_mfma_f32_32x32x16_f16 v[50:65], v[14:17], v[90:93], v[50:65]
	v_bitop3_b32 v14, v171, s26, v170 bitop3:0x36
	ds_read_b128 v[10:13], v14
	ds_read_b128 v[14:17], v14 offset:32768
	s_nop 7
	v_cvt_pk_f16_f32 v25, v24, v25
	v_cvt_pk_f16_f32 v24, v22, v23
	v_cvt_pk_f16_f32 v23, v20, v21
	v_cvt_pk_f16_f32 v22, v18, v19
	v_cvt_pk_f16_f32 v21, v32, v33
	s_waitcnt vmcnt(6) lgkmcnt(1)
	v_mfma_f32_32x32x16_f16 v[34:49], v[10:13], v[70:73], v[34:49]
	v_cvt_pk_f16_f32 v20, v30, v31
	v_cvt_pk_f16_f32 v19, v28, v29
	v_cvt_pk_f16_f32 v18, v26, v27
	ds_write_b128 v173, v[22:25]
	ds_write_b128 v172, v[18:21]
	v_cvt_pk_f16_f32 v21, v56, v57
	v_cvt_pk_f16_f32 v20, v54, v55
	s_waitcnt vmcnt(5)
	v_mfma_f32_32x32x16_f16 v[34:49], v[6:9], v[74:77], v[34:49]
	v_cvt_pk_f16_f32 v19, v52, v53
	v_cvt_pk_f16_f32 v18, v50, v51
	ds_write_b128 v173, v[18:21] offset:32768
	v_cvt_pk_f16_f32 v21, v64, v65
	v_cvt_pk_f16_f32 v20, v62, v63
	v_cvt_pk_f16_f32 v19, v60, v61
	v_cvt_pk_f16_f32 v18, v58, v59
	s_waitcnt vmcnt(4) lgkmcnt(3)
	v_mfma_f32_32x32x16_f16 v[34:49], v[14:17], v[78:81], v[34:49]
	ds_write_b128 v172, v[18:21] offset:32768
	s_waitcnt vmcnt(3)
	v_mfma_f32_32x32x16_f16 v[66:81], v[2:5], v[82:85], 0
	s_nop 8
	v_cvt_pk_f16_f32 v41, v40, v41
	v_cvt_pk_f16_f32 v40, v38, v39
	v_cvt_pk_f16_f32 v39, v36, v37
	v_cvt_pk_f16_f32 v38, v34, v35
	v_cvt_pk_f16_f32 v85, v48, v49
	v_cvt_pk_f16_f32 v84, v46, v47
	v_cvt_pk_f16_f32 v83, v44, v45
	s_waitcnt vmcnt(2)
	v_mfma_f32_32x32x16_f16 v[66:81], v[10:13], v[86:89], v[66:81]
	v_cvt_pk_f16_f32 v82, v42, v43
	s_waitcnt vmcnt(1)
	v_mfma_f32_32x32x16_f16 v[66:81], v[6:9], v[182:185], v[66:81]
	s_waitcnt vmcnt(0)
	v_mfma_f32_32x32x16_f16 v[66:81], v[14:17], v[186:189], v[66:81]
	v_mfma_f32_32x32x16_f16 v[2:17], v[38:41], v[126:129], 0
	s_nop 10
	v_cvt_pk_f16_f32 v73, v72, v73
	v_cvt_pk_f16_f32 v72, v70, v71
	v_cvt_pk_f16_f32 v70, v66, v67
	v_cvt_pk_f16_f32 v67, v76, v77
	v_cvt_pk_f16_f32 v66, v74, v75
	global_load_dwordx4 v[74:77], v154, s[2:3]
	v_cvt_pk_f16_f32 v71, v68, v69
	v_cvt_pk_f16_f32 v69, v80, v81
	v_cvt_pk_f16_f32 v68, v78, v79
	global_load_dwordx4 v[78:81], v154, s[2:3] offset:1024
	ds_read_b128 v[18:21], v180
	ds_read_b128 v[22:25], v176
	ds_read_b128 v[26:29], v180 offset:32768
	global_load_dwordx4 v[30:33], v154, s[2:3] offset:2048
	v_mfma_f32_32x32x16_f16 v[34:49], v[38:41], v[110:113], 0
	v_mfma_f32_32x32x16_f16 v[2:17], v[82:85], v[122:125], v[2:17]
	v_mfma_f32_32x32x16_f16 v[34:49], v[82:85], v[106:109], v[34:49]
	ds_read_b128 v[82:85], v176 offset:32768
	s_waitcnt vmcnt(2) lgkmcnt(3)
	v_mfma_f32_32x32x16_f16 v[50:65], v[18:21], v[74:77], 0
	v_mfma_f32_32x32x16_f16 v[2:17], v[70:73], v[118:121], v[2:17]
	v_mfma_f32_32x32x16_f16 v[34:49], v[70:73], v[94:97], v[34:49]
	v_lshl_add_u64 v[70:71], s[2:3], 0, v[154:155]
	v_add_co_u32_e32 v152, vcc, s23, v70
	s_nop 1
	v_addc_co_u32_e32 v153, vcc, 0, v71, vcc
	s_waitcnt vmcnt(1) lgkmcnt(2)
	v_mfma_f32_32x32x16_f16 v[50:65], v[22:25], v[78:81], v[50:65]
	v_mfma_f32_32x32x16_f16 v[2:17], v[66:69], v[114:117], v[2:17]
	v_mfma_f32_32x32x16_f16 v[34:49], v[66:69], v[90:93], v[34:49]
	global_load_dwordx4 v[66:69], v154, s[2:3] offset:3072
	s_nop 9
	v_cvt_pk_f16_f32 v9, v8, v9
	v_cvt_pk_f16_f32 v8, v6, v7
	v_cvt_pk_f16_f32 v7, v4, v5
	v_cvt_pk_f16_f32 v6, v2, v3
	v_cvt_pk_f16_f32 v5, v16, v17
	v_cvt_pk_f16_f32 v4, v14, v15
	s_waitcnt vmcnt(1) lgkmcnt(1)
	v_mfma_f32_32x32x16_f16 v[50:65], v[26:29], v[30:33], v[50:65]
	global_load_dwordx4 v[30:33], v168, s[2:3]
	global_load_dwordx4 v[86:89], v[152:153], off offset:1024
	s_nop 0
	global_load_dwordx4 v[168:171], v168, s[0:1]
	v_cvt_pk_f16_f32 v3, v12, v13
	v_cvt_pk_f16_f32 v2, v10, v11
	ds_write_b128 v175, v[6:9]
	ds_write_b128 v174, v[2:5]
	v_cvt_pk_f16_f32 v5, v40, v41
	s_waitcnt vmcnt(3) lgkmcnt(2)
	v_mfma_f32_32x32x16_f16 v[50:65], v[82:85], v[66:69], v[50:65]
	global_load_dwordx4 v[182:185], v154, s[0:1] offset:1024
	v_cvt_pk_f16_f32 v4, v38, v39
	v_cvt_pk_f16_f32 v3, v36, v37
	v_cvt_pk_f16_f32 v2, v34, v35
	ds_write_b128 v175, v[2:5] offset:32768
	v_cvt_pk_f16_f32 v5, v48, v49
	v_cvt_pk_f16_f32 v4, v46, v47
	s_waitcnt vmcnt(3)
	v_mfma_f32_32x32x16_f16 v[66:81], v[18:21], v[30:33], 0
	global_load_dwordx4 v[18:21], v[152:153], off offset:2048
	v_cvt_pk_f16_f32 v3, v44, v45
	v_cvt_pk_f16_f32 v2, v42, v43
	ds_write_b128 v174, v[2:5] offset:32768
	v_cvt_pk_f16_f32 v57, v56, v57
	v_cvt_pk_f16_f32 v56, v54, v55
	v_cvt_pk_f16_f32 v55, v52, v53
	s_waitcnt vmcnt(3)
	v_mfma_f32_32x32x16_f16 v[66:81], v[22:25], v[86:89], v[66:81]
	global_load_dwordx4 v[22:25], v[152:153], off offset:3072
	v_cvt_pk_f16_f32 v54, v50, v51
	s_waitcnt vmcnt(1)
	v_mfma_f32_32x32x16_f16 v[66:81], v[26:29], v[18:21], v[66:81]
	v_lshl_add_u64 v[18:19], s[0:1], 0, v[154:155]
	v_add_co_u32_e32 v152, vcc, s23, v18
	s_nop 1
	v_addc_co_u32_e32 v153, vcc, 0, v19, vcc
	global_load_dwordx4 v[86:89], v[152:153], off offset:1024
	s_waitcnt vmcnt(1)
	v_mfma_f32_32x32x16_f16 v[66:81], v[82:85], v[22:25], v[66:81]
	v_cvt_pk_f16_f32 v85, v64, v65
	v_cvt_pk_f16_f32 v84, v62, v63
	v_cvt_pk_f16_f32 v83, v60, v61
	v_cvt_pk_f16_f32 v82, v58, v59
	v_mfma_f32_32x32x16_f16 v[18:33], v[54:57], v[126:129], 0
	s_nop 6
	v_cvt_pk_f16_f32 v73, v72, v73
	v_cvt_pk_f16_f32 v72, v70, v71
	v_cvt_pk_f16_f32 v70, v66, v67
	v_cvt_pk_f16_f32 v67, v76, v77
	v_cvt_pk_f16_f32 v66, v74, v75
	global_load_dwordx4 v[74:77], v154, s[0:1]
	ds_read_b128 v[2:5], v181
	ds_read_b128 v[6:9], v177
	ds_read_b128 v[10:13], v181 offset:32768
	global_load_dwordx4 v[14:17], v154, s[0:1] offset:2048
	global_load_dwordx4 v[34:37], v154, s[0:1] offset:3072
	v_mfma_f32_32x32x16_f16 v[50:65], v[54:57], v[110:113], 0
	v_cvt_pk_f16_f32 v71, v68, v69
	v_cvt_pk_f16_f32 v69, v80, v81
	v_cvt_pk_f16_f32 v68, v78, v79
	v_mfma_f32_32x32x16_f16 v[18:33], v[82:85], v[122:125], v[18:33]
	v_mfma_f32_32x32x16_f16 v[50:65], v[82:85], v[106:109], v[50:65]
	ds_read_b128 v[82:85], v177 offset:32768
	v_mfma_f32_32x32x16_f16 v[18:33], v[70:73], v[118:121], v[18:33]
	v_mfma_f32_32x32x16_f16 v[50:65], v[70:73], v[94:97], v[50:65]
	v_mfma_f32_32x32x16_f16 v[18:33], v[66:69], v[114:117], v[18:33]
	v_mfma_f32_32x32x16_f16 v[50:65], v[66:69], v[90:93], v[50:65]
	s_nop 10
	v_cvt_pk_f16_f32 v25, v24, v25
	v_cvt_pk_f16_f32 v24, v22, v23
	v_cvt_pk_f16_f32 v23, v20, v21
	v_cvt_pk_f16_f32 v22, v18, v19
	ds_write_b128 v132, v[22:25]
	s_waitcnt vmcnt(2) lgkmcnt(4)
	v_mfma_f32_32x32x16_f16 v[66:81], v[2:5], v[74:77], 0
	s_waitcnt lgkmcnt(3)
	v_mfma_f32_32x32x16_f16 v[66:81], v[6:9], v[182:185], v[66:81]
	s_waitcnt vmcnt(1) lgkmcnt(2)
	v_mfma_f32_32x32x16_f16 v[66:81], v[10:13], v[14:17], v[66:81]
	s_waitcnt vmcnt(0) lgkmcnt(1)
	v_mfma_f32_32x32x16_f16 v[66:81], v[82:85], v[34:37], v[66:81]
	v_mfma_f32_32x32x16_f16 v[34:49], v[2:5], v[168:171], 0
	global_load_dwordx4 v[2:5], v[152:153], off offset:2048
	s_nop 9
	v_cvt_pk_f16_f32 v73, v72, v73
	v_cvt_pk_f16_f32 v72, v70, v71
	v_cvt_pk_f16_f32 v71, v68, v69
	v_cvt_pk_f16_f32 v70, v66, v67
	v_cvt_pk_f16_f32 v69, v80, v81
	v_cvt_pk_f16_f32 v68, v78, v79
	v_mfma_f32_32x32x16_f16 v[34:49], v[6:9], v[86:89], v[34:49]
	global_load_dwordx4 v[6:9], v[152:153], off offset:3072
	v_cvt_pk_f16_f32 v67, v76, v77
	v_cvt_pk_f16_f32 v66, v74, v75
	s_waitcnt vmcnt(1)
	v_mfma_f32_32x32x16_f16 v[34:49], v[10:13], v[2:5], v[34:49]
	s_waitcnt vmcnt(0)
	v_mfma_f32_32x32x16_f16 v[34:49], v[82:85], v[6:9], v[34:49]
	v_mfma_f32_32x32x16_f16 v[2:17], v[70:73], v[126:129], 0
	s_nop 10
	v_cvt_pk_f16_f32 v41, v40, v41
	v_cvt_pk_f16_f32 v40, v38, v39
	v_cvt_pk_f16_f32 v38, v34, v35
	v_cvt_pk_f16_f32 v35, v44, v45
	v_cvt_pk_f16_f32 v34, v42, v43
	v_cvt_pk_f16_f32 v45, v32, v33
	v_cvt_pk_f16_f32 v44, v30, v31
	v_cvt_pk_f16_f32 v43, v28, v29
	v_cvt_pk_f16_f32 v42, v26, v27
	v_mfma_f32_32x32x16_f16 v[18:33], v[70:73], v[110:113], 0
	v_cvt_pk_f16_f32 v39, v36, v37
	v_cvt_pk_f16_f32 v37, v48, v49
	v_cvt_pk_f16_f32 v36, v46, v47
	ds_write_b128 v131, v[42:45]
	v_cvt_pk_f16_f32 v45, v56, v57
	v_cvt_pk_f16_f32 v44, v54, v55
	v_cvt_pk_f16_f32 v43, v52, v53
	v_mfma_f32_32x32x16_f16 v[2:17], v[66:69], v[122:125], v[2:17]
	v_cvt_pk_f16_f32 v42, v50, v51
	ds_write_b128 v132, v[42:45] offset:32768
	v_cvt_pk_f16_f32 v45, v64, v65
	v_cvt_pk_f16_f32 v44, v62, v63
	v_cvt_pk_f16_f32 v43, v60, v61
	v_cvt_pk_f16_f32 v42, v58, v59
	ds_write_b128 v131, v[42:45] offset:32768
	v_mfma_f32_32x32x16_f16 v[18:33], v[66:69], v[106:109], v[18:33]
	v_mfma_f32_32x32x16_f16 v[2:17], v[38:41], v[118:121], v[2:17]
	v_mfma_f32_32x32x16_f16 v[18:33], v[38:41], v[94:97], v[18:33]
	v_mfma_f32_32x32x16_f16 v[2:17], v[34:37], v[114:117], v[2:17]
	v_mfma_f32_32x32x16_f16 v[18:33], v[34:37], v[90:93], v[18:33]
	s_nop 10
	v_cvt_pk_f16_f32 v9, v8, v9
	v_cvt_pk_f16_f32 v8, v6, v7
	v_cvt_pk_f16_f32 v7, v4, v5
	v_cvt_pk_f16_f32 v6, v2, v3
	v_cvt_pk_f16_f32 v5, v16, v17
	v_cvt_pk_f16_f32 v4, v14, v15
	v_cvt_pk_f16_f32 v3, v12, v13
	v_cvt_pk_f16_f32 v2, v10, v11
	ds_write_b128 v135, v[6:9]
	ds_write_b128 v133, v[2:5]
	v_cvt_pk_f16_f32 v5, v24, v25
	v_cvt_pk_f16_f32 v4, v22, v23
	v_cvt_pk_f16_f32 v3, v20, v21
	v_cvt_pk_f16_f32 v2, v18, v19
	ds_write_b128 v135, v[2:5] offset:32768
	v_cvt_pk_f16_f32 v5, v32, v33
	v_cvt_pk_f16_f32 v4, v30, v31
	v_cvt_pk_f16_f32 v3, v28, v29
	v_cvt_pk_f16_f32 v2, v26, v27
	ds_write_b128 v133, v[2:5] offset:32768
	s_setprio 0
	s_waitcnt lgkmcnt(0)
	s_barrier
	ds_read_b64_tr_b16 v[2:3], v146
	ds_read_b64_tr_b16 v[4:5], v147
	ds_read_b64_tr_b16 v[36:37], v147 offset:32768
	ds_read_b64_tr_b16 v[34:35], v146 offset:32768
	ds_read_b64_tr_b16 v[18:19], v150
	ds_read_b64_tr_b16 v[20:21], v151
	ds_read_b64_tr_b16 v[40:41], v151 offset:32768
	ds_read_b64_tr_b16 v[38:39], v150 offset:32768
	s_waitcnt lgkmcnt(6)
	v_mfma_f32_32x32x16_f16 v[2:17], v[2:5], v[102:105], 0
	ds_read_b64_tr_b16 v[42:43], v148
	ds_read_b64_tr_b16 v[44:45], v149
	ds_read_b64_tr_b16 v[48:49], v149 offset:32768
	ds_read_b64_tr_b16 v[46:47], v148 offset:32768
	v_cmp_gt_u32_e64 s[0:1], 32, v167
	s_cmp_eq_u32 s5, 0
	v_cmp_lt_i32_e64 s[2:3], v162, v163
	s_waitcnt lgkmcnt(6)
	v_mfma_f32_32x32x16_f16 v[18:33], v[18:21], v[102:105], 0
	v_mfma_f32_32x32x16_f16 v[2:17], v[34:37], v[98:101], v[2:17]
	s_waitcnt lgkmcnt(4)
	v_mfma_f32_32x32x16_f16 v[18:33], v[38:41], v[98:101], v[18:33]
	s_nop 9
	v_mul_f32_e64 v34, v16, v16
	v_mul_f32_e64 v35, v17, v17
	v_mul_f32_e64 v36, v12, v12
	v_mul_f32_e64 v37, v13, v13
	v_mul_f32_e64 v50, v8, v8
	v_mul_f32_e64 v51, v9, v9
	v_pk_mul_f32 v[52:53], v[4:5], v[4:5]
	v_pk_fma_f32 v[50:51], v[6:7], v[6:7], v[50:51]
	v_pk_fma_f32 v[52:53], v[2:3], v[2:3], v[52:53]
	v_pk_fma_f32 v[36:37], v[10:11], v[10:11], v[36:37]
	v_pk_fma_f32 v[34:35], v[14:15], v[14:15], v[34:35]
	v_pk_mul_f32 v[116:117], v[24:25], v[24:25]
	v_pk_mul_f32 v[118:119], v[20:21], v[20:21]
	v_pk_add_f32 v[50:51], v[52:53], v[50:51]
	v_pk_add_f32 v[34:35], v[36:37], v[34:35]
	v_pk_mul_f32 v[112:113], v[32:33], v[32:33]
	v_pk_mul_f32 v[114:115], v[28:29], v[28:29]
	v_pk_mul_f32 v[120:121], v[18:19], v[18:19]
	v_pk_fma_f32 v[18:19], v[18:19], v[18:19], v[118:119]
	v_pk_fma_f32 v[20:21], v[22:23], v[22:23], v[116:117]
	v_pk_add_f32 v[34:35], v[50:51], v[34:35]
	v_pk_mul_f32 v[106:107], v[22:23], v[22:23]
	v_pk_add_f32 v[18:19], v[18:19], v[20:21]
	v_pk_fma_f32 v[20:21], v[26:27], v[26:27], v[114:115]
	v_pk_fma_f32 v[22:23], v[30:31], v[30:31], v[112:113]
	v_add_f32_e32 v34, v34, v35
	v_pk_add_f32 v[20:21], v[20:21], v[22:23]
	v_add_f32_e32 v36, 0, v34
	v_pk_mul_f32 v[108:109], v[26:27], v[26:27]
	v_pk_mul_f32 v[110:111], v[30:31], v[30:31]
	v_pk_add_f32 v[34:35], v[18:19], v[20:21]
	s_waitcnt lgkmcnt(2)
	v_mfma_f32_32x32x16_f16 v[18:33], v[42:45], v[102:105], 0
	v_add_f32_e32 v34, v34, v35
	v_add_f32_e32 v54, v36, v34
	v_sub_f32_e32 v55, v36, v34
	ds_read_b64_tr_b16 v[34:35], v144
	ds_read_b64_tr_b16 v[36:37], v145
	ds_read_b64_tr_b16 v[52:53], v145 offset:32768
	ds_read_b64_tr_b16 v[50:51], v144 offset:32768
	v_pk_fma_f32 v[4:5], v[4:5], v[4:5], v[118:119]
	v_pk_fma_f32 v[16:17], v[16:17], v[16:17], v[112:113]
	v_pk_fma_f32 v[14:15], v[14:15], v[14:15], v[110:111]
	s_waitcnt lgkmcnt(4)
	v_mfma_f32_32x32x16_f16 v[18:33], v[46:49], v[98:101], v[18:33]
	v_fma_f32 v12, v12, v12, v114
	v_fma_f32 v13, v13, v13, v115
	v_fma_f32 v10, v10, v10, v108
	v_fma_f32 v11, v11, v11, v109
	v_fma_f32 v8, v8, v8, v116
	v_fma_f32 v9, v9, v9, v117
	v_pk_fma_f32 v[6:7], v[6:7], v[6:7], v[106:107]
	v_pk_fma_f32 v[2:3], v[2:3], v[2:3], v[120:121]
	s_nop 3
	v_pk_mul_f32 v[38:39], v[32:33], v[32:33]
	v_pk_mul_f32 v[40:41], v[28:29], v[28:29]
	v_pk_mul_f32 v[42:43], v[24:25], v[24:25]
	v_pk_mul_f32 v[44:45], v[20:21], v[20:21]
	v_pk_fma_f32 v[42:43], v[22:23], v[22:23], v[42:43]
	v_pk_fma_f32 v[44:45], v[18:19], v[18:19], v[44:45]
	v_pk_fma_f32 v[40:41], v[26:27], v[26:27], v[40:41]
	v_pk_fma_f32 v[38:39], v[30:31], v[30:31], v[38:39]
	v_pk_add_f32 v[42:43], v[44:45], v[42:43]
	v_pk_add_f32 v[38:39], v[40:41], v[38:39]
	v_pk_fma_f32 v[4:5], v[20:21], v[20:21], v[4:5]
	v_pk_add_f32 v[38:39], v[42:43], v[38:39]
	v_pk_fma_f32 v[6:7], v[22:23], v[22:23], v[6:7]
	v_add_f32_e32 v56, v38, v39
	s_waitcnt lgkmcnt(2)
	v_mfma_f32_32x32x16_f16 v[34:49], v[34:37], v[102:105], 0
	v_add_f32_e32 v70, v54, v56
	v_add_f32_e32 v71, v55, v56
	v_sub_f32_e32 v72, v54, v56
	ds_read_b64_tr_b16 v[54:55], v142
	ds_read_b64_tr_b16 v[56:57], v143
	ds_read_b64_tr_b16 v[68:69], v143 offset:32768
	ds_read_b64_tr_b16 v[66:67], v142 offset:32768
	v_pk_fma_f32 v[8:9], v[24:25], v[24:25], v[8:9]
	v_pk_fma_f32 v[10:11], v[26:27], v[26:27], v[10:11]
	v_pk_fma_f32 v[12:13], v[28:29], v[28:29], v[12:13]
	s_waitcnt lgkmcnt(4)
	v_mfma_f32_32x32x16_f16 v[34:49], v[50:53], v[98:101], v[34:49]
	v_fma_f32 v14, v30, v30, v14
	v_fma_f32 v15, v31, v31, v15
	v_fma_f32 v16, v32, v32, v16
	v_fma_f32 v17, v33, v33, v17
	v_fma_f32 v2, v18, v18, v2
	v_fma_f32 v3, v19, v19, v3
	s_nop 5
	v_pk_mul_f32 v[50:51], v[48:49], v[48:49]
	v_pk_mul_f32 v[52:53], v[44:45], v[44:45]
	v_pk_mul_f32 v[58:59], v[40:41], v[40:41]
	v_pk_mul_f32 v[60:61], v[36:37], v[36:37]
	v_pk_fma_f32 v[58:59], v[38:39], v[38:39], v[58:59]
	v_pk_fma_f32 v[60:61], v[34:35], v[34:35], v[60:61]
	v_pk_fma_f32 v[52:53], v[42:43], v[42:43], v[52:53]
	v_pk_fma_f32 v[50:51], v[46:47], v[46:47], v[50:51]
	v_pk_add_f32 v[58:59], v[60:61], v[58:59]
	v_pk_add_f32 v[50:51], v[52:53], v[50:51]
	v_pk_fma_f32 v[4:5], v[36:37], v[36:37], v[4:5]
	v_pk_add_f32 v[50:51], v[58:59], v[50:51]
	v_pk_fma_f32 v[16:17], v[48:49], v[48:49], v[16:17]
	v_add_f32_e32 v73, v50, v51
	s_waitcnt lgkmcnt(2)
	v_mfma_f32_32x32x16_f16 v[50:65], v[54:57], v[102:105], 0
	v_add_f32_e32 v86, v70, v73
	v_sub_f32_e32 v87, v71, v73
	v_sub_f32_e32 v88, v72, v73
	ds_read_b64_tr_b16 v[70:71], v140
	ds_read_b64_tr_b16 v[72:73], v141
	ds_read_b64_tr_b16 v[84:85], v141 offset:32768
	ds_read_b64_tr_b16 v[82:83], v140 offset:32768
	v_pk_fma_f32 v[14:15], v[46:47], v[46:47], v[14:15]
	v_pk_fma_f32 v[12:13], v[44:45], v[44:45], v[12:13]
	v_pk_fma_f32 v[10:11], v[42:43], v[42:43], v[10:11]
	s_waitcnt lgkmcnt(4)
	v_mfma_f32_32x32x16_f16 v[50:65], v[66:69], v[98:101], v[50:65]
	v_fma_f32 v8, v40, v40, v8
	v_fma_f32 v9, v41, v41, v9
	v_fma_f32 v6, v38, v38, v6
	v_fma_f32 v7, v39, v39, v7
	v_fma_f32 v2, v34, v34, v2
	v_fma_f32 v3, v35, v35, v3
	s_nop 5
	v_pk_mul_f32 v[66:67], v[64:65], v[64:65]
	v_pk_mul_f32 v[68:69], v[60:61], v[60:61]
	v_pk_mul_f32 v[74:75], v[56:57], v[56:57]
	v_pk_mul_f32 v[76:77], v[52:53], v[52:53]
	v_pk_fma_f32 v[74:75], v[54:55], v[54:55], v[74:75]
	v_pk_fma_f32 v[76:77], v[50:51], v[50:51], v[76:77]
	v_pk_fma_f32 v[68:69], v[58:59], v[58:59], v[68:69]
	v_pk_fma_f32 v[66:67], v[62:63], v[62:63], v[66:67]
	v_pk_add_f32 v[74:75], v[76:77], v[74:75]
	v_pk_add_f32 v[66:67], v[68:69], v[66:67]
	v_pk_fma_f32 v[4:5], v[52:53], v[52:53], v[4:5]
	v_pk_add_f32 v[66:67], v[74:75], v[66:67]
	v_pk_fma_f32 v[6:7], v[54:55], v[54:55], v[6:7]
	v_add_f32_e32 v89, v66, v67
	s_waitcnt lgkmcnt(2)
	v_mfma_f32_32x32x16_f16 v[66:81], v[70:73], v[102:105], 0
	v_add_f32_e32 v94, v86, v89
	v_add_f32_e32 v126, v87, v89
	v_add_f32_e32 v127, v88, v89
	v_sub_f32_e32 v128, v86, v89
	ds_read_b64_tr_b16 v[86:87], v138
	ds_read_b64_tr_b16 v[88:89], v139
	ds_read_b64_tr_b16 v[124:125], v139 offset:32768
	ds_read_b64_tr_b16 v[122:123], v138 offset:32768
	v_pk_fma_f32 v[8:9], v[56:57], v[56:57], v[8:9]
	v_pk_fma_f32 v[10:11], v[58:59], v[58:59], v[10:11]
	s_waitcnt lgkmcnt(4)
	v_mfma_f32_32x32x16_f16 v[66:81], v[82:85], v[98:101], v[66:81]
	v_fma_f32 v12, v60, v60, v12
	v_fma_f32 v13, v61, v61, v13
	v_fma_f32 v14, v62, v62, v14
	v_fma_f32 v15, v63, v63, v15
	v_fma_f32 v16, v64, v64, v16
	v_fma_f32 v17, v65, v65, v17
	v_pk_fma_f32 v[2:3], v[50:51], v[50:51], v[2:3]
	s_nop 4
	v_pk_mul_f32 v[82:83], v[80:81], v[80:81]
	v_pk_mul_f32 v[84:85], v[76:77], v[76:77]
	v_pk_mul_f32 v[90:91], v[72:73], v[72:73]
	v_pk_mul_f32 v[92:93], v[68:69], v[68:69]
	v_pk_fma_f32 v[90:91], v[70:71], v[70:71], v[90:91]
	v_pk_fma_f32 v[92:93], v[66:67], v[66:67], v[92:93]
	v_pk_fma_f32 v[84:85], v[74:75], v[74:75], v[84:85]
	v_pk_fma_f32 v[82:83], v[78:79], v[78:79], v[82:83]
	v_pk_add_f32 v[90:91], v[92:93], v[90:91]
	v_pk_add_f32 v[82:83], v[84:85], v[82:83]
	v_pk_fma_f32 v[4:5], v[68:69], v[68:69], v[4:5]
	v_pk_add_f32 v[82:83], v[90:91], v[82:83]
	v_pk_fma_f32 v[18:19], v[80:81], v[80:81], v[16:17]
	v_add_f32_e32 v129, v82, v83
	v_add_f32_e32 v131, v94, v129
	s_waitcnt lgkmcnt(2)
	v_mfma_f32_32x32x16_f16 v[82:97], v[86:89], v[102:105], 0
	v_sub_f32_e32 v135, v126, v129
	v_add_f32_e32 v142, v127, v129
	v_sub_f32_e32 v143, v128, v129
	ds_read_b64_tr_b16 v[126:127], v136
	ds_read_b64_tr_b16 v[128:129], v137
	ds_read_b64_tr_b16 v[138:139], v137 offset:32768
	ds_read_b64_tr_b16 v[136:137], v136 offset:32768
	v_pk_fma_f32 v[20:21], v[78:79], v[78:79], v[14:15]
	v_pk_fma_f32 v[22:23], v[76:77], v[76:77], v[12:13]
	v_pk_fma_f32 v[24:25], v[74:75], v[74:75], v[10:11]
	s_waitcnt lgkmcnt(4)
	v_mfma_f32_32x32x16_f16 v[82:97], v[122:125], v[98:101], v[82:97]
	v_fma_f32 v26, v72, v72, v8
	v_fma_f32 v27, v73, v73, v9
	v_fma_f32 v28, v70, v70, v6
	v_fma_f32 v29, v71, v71, v7
	v_fma_f32 v30, v66, v66, v2
	v_fma_f32 v31, v67, v67, v3
	s_nop 5
	v_pk_fma_f32 v[32:33], v[84:85], v[84:85], v[4:5]
	s_waitcnt lgkmcnt(2)
	v_mfma_f32_32x32x16_f16 v[2:17], v[126:129], v[102:105], 0
	v_fma_f32 v28, v86, v86, v28
	v_fma_f32 v29, v87, v87, v29
	v_fma_f32 v24, v90, v90, v24
	v_fma_f32 v25, v91, v91, v25
	v_fma_f32 v22, v92, v92, v22
	v_fma_f32 v23, v93, v93, v23
	v_pk_fma_f32 v[20:21], v[94:95], v[94:95], v[20:21]
	v_pk_fma_f32 v[18:19], v[96:97], v[96:97], v[18:19]
	v_pk_fma_f32 v[30:31], v[82:83], v[82:83], v[30:31]
	v_pk_fma_f32 v[26:27], v[88:89], v[88:89], v[26:27]
	s_waitcnt lgkmcnt(0)
	v_mfma_f32_32x32x16_f16 v[2:17], v[136:139], v[98:101], v[2:17]
	v_mul_f32_e64 v122, v96, v96
	v_mul_f32_e64 v123, v97, v97
	v_mul_f32_e64 v124, v92, v92
	v_mul_f32_e64 v125, v93, v93
	v_mul_f32_e64 v132, v88, v88
	v_mul_f32_e64 v133, v89, v89
	v_pk_mul_f32 v[140:141], v[84:85], v[84:85]
	v_pk_fma_f32 v[132:133], v[86:87], v[86:87], v[132:133]
	v_pk_fma_f32 v[140:141], v[82:83], v[82:83], v[140:141]
	v_pk_fma_f32 v[124:125], v[90:91], v[90:91], v[124:125]
	s_nop 1
	v_pk_mul_f32 v[38:39], v[8:9], v[8:9]
	v_pk_mul_f32 v[40:41], v[4:5], v[4:5]
	v_pk_mul_f32 v[34:35], v[16:17], v[16:17]
	v_pk_mul_f32 v[36:37], v[12:13], v[12:13]
	v_pk_fma_f32 v[16:17], v[16:17], v[16:17], v[18:19]
	v_pk_fma_f32 v[18:19], v[14:15], v[14:15], v[20:21]
	v_pk_fma_f32 v[12:13], v[12:13], v[12:13], v[22:23]
	v_pk_fma_f32 v[20:21], v[10:11], v[10:11], v[24:25]
	v_pk_fma_f32 v[22:23], v[6:7], v[6:7], v[28:29]
	v_pk_fma_f32 v[24:25], v[2:3], v[2:3], v[30:31]
	v_pk_fma_f32 v[2:3], v[2:3], v[2:3], v[40:41]
	v_pk_fma_f32 v[6:7], v[6:7], v[6:7], v[38:39]
	v_pk_fma_f32 v[4:5], v[4:5], v[4:5], v[32:33]
	v_pk_add_f32 v[2:3], v[2:3], v[6:7]
	v_pk_fma_f32 v[6:7], v[10:11], v[10:11], v[36:37]
	v_pk_fma_f32 v[10:11], v[14:15], v[14:15], v[34:35]
	v_pk_fma_f32 v[8:9], v[8:9], v[8:9], v[26:27]
	v_pk_add_f32 v[6:7], v[6:7], v[10:11]
	v_sub_f32_e32 v10, v24, v25
	v_add_f32_e32 v11, v25, v24
	v_add_f32_e32 v10, v4, v10
	v_sub_f32_e32 v14, v11, v4
	v_add_f32_e32 v4, v4, v11
	v_sub_f32_e32 v10, v10, v5
	v_sub_f32_e32 v11, v14, v5
	v_add_f32_e32 v4, v5, v4
	v_add_f32_e32 v5, v22, v10
	v_add_f32_e32 v10, v22, v11
	v_sub_f32_e32 v11, v4, v22
	v_add_f32_e32 v4, v22, v4
	v_sub_f32_e32 v5, v5, v23
	v_add_f32_e32 v10, v23, v10
	v_sub_f32_e32 v11, v11, v23
	v_add_f32_e32 v4, v23, v4
	v_add_f32_e32 v5, v8, v5
	v_sub_f32_e32 v10, v10, v8
	v_sub_f32_e32 v11, v11, v8
	v_add_f32_e32 v4, v8, v4
	v_sub_f32_e32 v5, v5, v9
	v_pk_fma_f32 v[122:123], v[94:95], v[94:95], v[122:123]
	v_sub_f32_e32 v8, v10, v9
	v_sub_f32_e32 v10, v11, v9
	v_add_f32_e32 v4, v9, v4
	v_add_f32_e32 v5, v20, v5
	v_pk_add_f32 v[132:133], v[140:141], v[132:133]
	v_pk_add_f32 v[122:123], v[124:125], v[122:123]
	v_add_f32_e32 v8, v20, v8
	v_add_f32_e32 v9, v20, v10
	v_sub_f32_e32 v4, v4, v20
	v_sub_f32_e32 v5, v5, v21
	v_pk_add_f32 v[122:123], v[132:133], v[122:123]
	v_add_f32_e32 v8, v21, v8
	v_add_f32_e32 v9, v21, v9
	v_sub_f32_e32 v4, v4, v21
	v_add_f32_e32 v5, v12, v5
	v_add_f32_e32 v122, v122, v123
	v_pk_add_f32 v[2:3], v[2:3], v[6:7]
	v_sub_f32_e32 v8, v8, v12
	v_add_f32_e32 v9, v12, v9
	v_sub_f32_e32 v4, v4, v12
	v_sub_f32_e32 v5, v5, v13
	v_add_f32_e32 v123, v131, v122
	v_add_f32_e32 v2, v2, v3
	v_sub_f32_e32 v8, v8, v13
	v_add_f32_e32 v9, v13, v9
	v_sub_f32_e32 v4, v4, v13
	v_add_f32_e32 v5, v18, v5
	v_add_f32_e32 v3, v123, v2
	v_add_f32_e32 v8, v18, v8
	v_sub_f32_e32 v9, v9, v18
	v_sub_f32_e32 v4, v4, v18
	v_sub_f32_e32 v5, v5, v19
	v_and_b32_e32 v10, 8, v156
	v_add_f32_e32 v8, v19, v8
	v_sub_f32_e32 v9, v9, v19
	v_sub_f32_e32 v4, v4, v19
	v_add_f32_e32 v5, v16, v5
	v_cmp_eq_u32_e32 vcc, 0, v10
	v_cndmask_b32_e64 v10, -v3, v3, s[0:1]
	s_cselect_b64 s[0:1], -1, 0
	s_bitcmp0_b32 s4, 7
	v_sub_f32_e32 v8, v8, v16
	v_sub_f32_e32 v9, v9, v16
	v_sub_f32_e32 v4, v4, v16
	v_sub_f32_e32 v5, v5, v17
	v_cndmask_b32_e64 v11, -v3, v3, s[0:1]
	s_cselect_b64 s[0:1], -1, 0
	v_and_b32_e32 v16, 32, v156
	v_sub_f32_e32 v8, v8, v17
	v_cndmask_b32_e64 v5, -v5, v5, vcc
	v_cndmask_b32_e64 v12, -v3, v3, s[0:1]
	v_cndmask_b32_e64 v18, v161, v162, s[2:3]
	v_cmp_eq_u32_e64 s[2:3], 0, v16
	v_lshlrev_b32_e32 v18, 2, v18
	v_cmp_eq_u32_e64 s[0:1], 0, v134
	v_cndmask_b32_e64 v16, v11, v5, s[2:3]
	v_cndmask_b32_e64 v5, v5, v11, s[2:3]
	v_cndmask_b32_e64 v11, v8, v12, s[2:3]
	ds_bpermute_b32 v11, v18, v11
	v_and_b32_e32 v14, 2, v156
	v_cndmask_b32_e64 v13, -v3, v3, s[0:1]
	v_cmp_eq_u32_e64 s[0:1], 0, v14
	v_cndmask_b32_e64 v8, v12, v8, s[2:3]
	v_add_f32_e32 v124, v135, v122
	v_cndmask_b32_e64 v14, -v3, v3, s[0:1]
	v_cmp_eq_u32_e64 s[0:1], 0, v130
	v_sub_f32_e32 v4, v4, v17
	s_waitcnt lgkmcnt(0)
	v_add_f32_e32 v8, v8, v11
	v_cndmask_b32_e64 v15, -v3, v3, s[0:1]
	v_cndmask_b32_e64 v11, v14, v10, s[2:3]
	v_cndmask_b32_e64 v10, v10, v14, s[2:3]
	v_sub_f32_e32 v6, v124, v2
	v_sub_f32_e32 v9, v9, v17
	v_cndmask_b32_e64 v3, -v3, v3, vcc
	ds_bpermute_b32 v10, v18, v10
	v_cndmask_b32_e64 v12, v4, v15, s[2:3]
	v_sub_f32_e32 v125, v142, v122
	v_cndmask_b32_e64 v19, v9, v13, s[2:3]
	v_cndmask_b32_e64 v9, v13, v9, s[2:3]
	ds_bpermute_b32 v12, v18, v12
	v_cndmask_b32_e64 v13, v6, v3, s[2:3]
	v_sub_f32_e32 v7, v125, v2
	v_bfe_i32 v17, v156, 5, 1
	ds_bpermute_b32 v5, v18, v5
	ds_bpermute_b32 v13, v18, v13
	v_sub_f32_e32 v122, v143, v122
	v_cndmask_b32_e64 v3, v3, v6, s[2:3]
	v_and_b32_e32 v6, v17, v7
	v_sub_f32_e32 v2, v122, v2
	ds_bpermute_b32 v19, v18, v19
	ds_bpermute_b32 v6, v18, v6
	s_waitcnt lgkmcnt(5)
	v_add_f32_e32 v10, v11, v10
	v_cndmask_b32_e64 v4, v15, v4, s[2:3]
	v_and_b32_e32 v11, v17, v2
	s_waitcnt lgkmcnt(4)
	v_add_f32_e32 v4, v4, v12
	ds_bpermute_b32 v11, v18, v11
	v_and_b32_e32 v12, 16, v156
	v_cmp_lt_i32_e64 s[4:5], v164, v163
	s_waitcnt lgkmcnt(4)
	v_add_f32_e32 v5, v16, v5
	s_waitcnt lgkmcnt(3)
	v_add_f32_e32 v3, v3, v13
	v_cndmask_b32_e64 v13, v161, v164, s[4:5]
	v_cmp_eq_u32_e64 s[4:5], 0, v12
	s_waitcnt lgkmcnt(2)
	v_add_f32_e32 v9, v9, v19
	v_lshlrev_b32_e32 v13, 2, v13
	v_cndmask_b32_e64 v12, v4, v5, s[4:5]
	v_cndmask_b32_e64 v4, v5, v4, s[4:5]
	v_cndmask_b32_e64 v5, 0, v7, s[2:3]
	s_waitcnt lgkmcnt(1)
	v_add_f32_e32 v5, v5, v6
	v_cndmask_b32_e64 v2, 0, v2, s[2:3]
	v_cndmask_b32_e64 v7, v9, v5, s[4:5]
	ds_bpermute_b32 v4, v13, v4
	s_waitcnt lgkmcnt(1)
	v_add_f32_e32 v2, v2, v11
	v_cndmask_b32_e64 v6, v3, v8, s[4:5]
	v_cndmask_b32_e64 v3, v8, v3, s[4:5]
	ds_bpermute_b32 v7, v13, v7
	ds_bpermute_b32 v3, v13, v3
	v_cndmask_b32_e64 v8, v10, v2, s[4:5]
	ds_bpermute_b32 v8, v13, v8
	v_cndmask_b32_e64 v5, v5, v9, s[4:5]
	s_waitcnt lgkmcnt(3)
	v_add_f32_e32 v4, v12, v4
	s_waitcnt lgkmcnt(2)
	v_add_f32_e32 v5, v5, v7
	s_waitcnt lgkmcnt(1)
	v_add_f32_e32 v3, v6, v3
	v_cndmask_b32_e64 v2, v2, v10, s[4:5]
	v_cndmask_b32_e32 v6, v5, v4, vcc
	v_cndmask_b32_e32 v4, v4, v5, vcc
	v_mov_b32_e32 v5, v155
	s_waitcnt lgkmcnt(0)
	v_add_f32_e32 v2, v2, v8
	v_mov_b32_dpp v5, v4 row_mirror row_mask:0xf bank_mask:0xf
	s_nop 1
	v_add_f32_dpp v4, v5, v6 row_half_mirror row_mask:0xf bank_mask:0xf bound_ctrl:1
	v_cndmask_b32_e32 v5, v2, v3, vcc
	v_cndmask_b32_e32 v2, v3, v2, vcc
	v_mov_b32_e32 v3, v155
	s_nop 1
	v_mov_b32_dpp v3, v2 row_mirror row_mask:0xf bank_mask:0xf
	s_nop 1
	v_add_f32_dpp v2, v3, v5 row_half_mirror row_mask:0xf bank_mask:0xf bound_ctrl:1
	v_cndmask_b32_e64 v3, v2, v4, s[0:1]
	v_cndmask_b32_e64 v2, v4, v2, s[0:1]
	v_mov_b32_e32 v4, v155
	s_nop 1
	v_mov_b32_dpp v4, v2 row_half_mirror row_mask:0xf bank_mask:0xf
	s_nop 1
	v_add_f32_dpp v2, v4, v3 quad_perm:[3,2,1,0] row_mask:0xf bank_mask:0xf bound_ctrl:1
	v_and_b32_e32 v4, 3, v156
	v_cmp_eq_u32_e32 vcc, 0, v4
	v_and_b32_e32 v4, 56, v156
	v_add_f32_dpp v2, v2, v2 quad_perm:[2,3,0,1] row_mask:0xf bank_mask:0xf bound_ctrl:1
	v_mov_b32_e32 v3, 0
	v_cmp_ne_u32_e64 s[0:1], 56, v4
	s_and_b64 s[2:3], vcc, s[0:1]
	v_mov_b32_dpp v3, v2 quad_perm:[1,0,3,2] row_mask:0xf bank_mask:0xf
	s_and_saveexec_b64 s[0:1], s[2:3]
	v_and_b32_e32 v4, 0xfc, v156
	v_add_f32_e32 v2, v2, v3
	v_or_b32_e32 v4, v165, v4
	ds_write_b32 v4, v2
	s_or_b64 exec, exec, s[0:1]
	v_cmp_gt_i32_e32 vcc, 14, v156
	s_waitcnt lgkmcnt(0)
	s_barrier
	s_and_saveexec_b64 s[0:1], vcc
	s_cbranch_execz .LBB1_2
	ds_read_b32 v2, v166
	ds_read_b32 v3, v166 offset:64
	ds_read_b32 v4, v166 offset:128
	ds_read_b32 v5, v166 offset:192
	s_waitcnt lgkmcnt(2)
	v_add_f32_e32 v2, v2, v3
	s_waitcnt lgkmcnt(1)
	v_add_f32_e32 v2, v2, v4
	s_waitcnt lgkmcnt(0)
	v_add_f32_e32 v2, v2, v5
	v_mul_f32_e32 v4, 0x39800000, v2
	v_lshl_add_u64 v[2:3], v[156:157], 2, s[14:15]
	global_store_dword v[2:3], v4, off
	s_branch .LBB1_2
